# GEMM K loops: loop-counter bumps and exit compare moved in front of the trip's last barrier (back-edge rotation, branch stays), on top of v102
# speedup vs baseline: 1.0184x; 1.0071x over previous
.LBB0_426:
	ds_read_b128 v[134:137], v132
	ds_read_b128 v[138:141], v132 offset:1024
	ds_read_b128 v[142:145], v132 offset:2048
	ds_read_b128 v[146:149], v132 offset:3072
	ds_read_b128 v[150:153], v132 offset:16384
	ds_read_b128 v[154:157], v132 offset:17408
	ds_read_b128 v[158:161], v132 offset:18432
	ds_read_b128 v[162:165], v132 offset:19456
	s_add_i32 s6, s41, 0xfffa0080
	s_cmp_eq_u32 s43, 12
	s_cselect_b32 s45, s39, s42
	s_cselect_b32 s44, s40, s6
	s_or_b32 s46, s45, 0x80
	s_add_i32 s6, s41, 0xfffe0000
	s_mov_b32 m0, s27
	ds_read_b128 v[166:169], v133
	ds_read_b128 v[170:173], v133 offset:1024
	ds_read_b128 v[174:177], v133 offset:2048
	ds_read_b128 v[178:181], v133 offset:3072
	ds_read_b128 v[182:185], v133 offset:4096
	ds_read_b128 v[186:189], v133 offset:5120
	ds_read_b128 v[190:193], v133 offset:6144
	ds_read_b128 v[194:197], v133 offset:7168
	buffer_load_dwordx4 v129, s[60:63], s6 offen lds
	s_mov_b32 m0, s28
	s_nop 0
	buffer_load_dwordx4 v129, s[60:63], s41 offen lds
	s_waitcnt vmcnt(8)
	s_waitcnt lgkmcnt(0)
	s_barrier
	s_setprio 1
	s_waitcnt lgkmcnt(0)
	v_mfma_f32_16x16x32_bf16 v[124:127], v[134:137], v[166:169], v[124:127]
	v_mfma_f32_16x16x32_bf16 v[120:123], v[142:145], v[166:169], v[120:123]
	s_waitcnt lgkmcnt(5)
	v_mfma_f32_16x16x32_bf16 v[116:119], v[134:137], v[174:177], v[116:119]
	v_mfma_f32_16x16x32_bf16 v[112:115], v[142:145], v[174:177], v[112:115]
	s_waitcnt lgkmcnt(3)
	v_mfma_f32_16x16x32_bf16 v[100:103], v[134:137], v[182:185], v[100:103]
	v_mfma_f32_16x16x32_bf16 v[96:99], v[142:145], v[182:185], v[96:99]
	s_waitcnt lgkmcnt(1)
	v_mfma_f32_16x16x32_bf16 v[84:87], v[134:137], v[190:193], v[84:87]
	v_mfma_f32_16x16x32_bf16 v[80:83], v[142:145], v[190:193], v[80:83]
	v_mfma_f32_16x16x32_bf16 v[124:127], v[138:141], v[170:173], v[124:127]
	v_mfma_f32_16x16x32_bf16 v[120:123], v[146:149], v[170:173], v[120:123]
	v_mfma_f32_16x16x32_bf16 v[116:119], v[138:141], v[178:181], v[116:119]
	v_mfma_f32_16x16x32_bf16 v[112:115], v[146:149], v[178:181], v[112:115]
	v_mfma_f32_16x16x32_bf16 v[100:103], v[138:141], v[186:189], v[100:103]
	v_mfma_f32_16x16x32_bf16 v[96:99], v[146:149], v[186:189], v[96:99]
	s_waitcnt lgkmcnt(0)
	v_mfma_f32_16x16x32_bf16 v[84:87], v[138:141], v[194:197], v[84:87]
	v_mfma_f32_16x16x32_bf16 v[80:83], v[146:149], v[194:197], v[80:83]
	s_setprio 0
	s_setprio 1
	v_mfma_f32_16x16x32_bf16 v[108:111], v[150:153], v[166:169], v[108:111]
	v_mfma_f32_16x16x32_bf16 v[104:107], v[158:161], v[166:169], v[104:107]
	v_mfma_f32_16x16x32_bf16 v[92:95], v[150:153], v[174:177], v[92:95]
	v_mfma_f32_16x16x32_bf16 v[88:91], v[158:161], v[174:177], v[88:91]
	v_mfma_f32_16x16x32_bf16 v[76:79], v[150:153], v[182:185], v[76:79]
	v_mfma_f32_16x16x32_bf16 v[72:75], v[158:161], v[182:185], v[72:75]
	v_mfma_f32_16x16x32_bf16 v[68:71], v[150:153], v[190:193], v[68:71]
	v_mfma_f32_16x16x32_bf16 v[64:67], v[158:161], v[190:193], v[64:67]
	v_mfma_f32_16x16x32_bf16 v[108:111], v[154:157], v[170:173], v[108:111]
	v_mfma_f32_16x16x32_bf16 v[104:107], v[162:165], v[170:173], v[104:107]
	v_mfma_f32_16x16x32_bf16 v[92:95], v[154:157], v[178:181], v[92:95]
	v_mfma_f32_16x16x32_bf16 v[88:91], v[162:165], v[178:181], v[88:91]
	v_mfma_f32_16x16x32_bf16 v[76:79], v[154:157], v[186:189], v[76:79]
	v_mfma_f32_16x16x32_bf16 v[72:75], v[162:165], v[186:189], v[72:75]
	v_mfma_f32_16x16x32_bf16 v[68:71], v[154:157], v[194:197], v[68:71]
	v_mfma_f32_16x16x32_bf16 v[64:67], v[162:165], v[194:197], v[64:67]
	s_setprio 0
	s_barrier
	s_mov_b32 m0, s13
	s_mov_b32 s6, s62
	s_mov_b32 s7, s63
	ds_read_b128 v[166:169], v133 offset:16384
	ds_read_b128 v[170:173], v133 offset:17408
	ds_read_b128 v[174:177], v133 offset:18432
	ds_read_b128 v[178:181], v133 offset:19456
	ds_read_b128 v[182:185], v133 offset:20480
	ds_read_b128 v[186:189], v133 offset:21504
	ds_read_b128 v[190:193], v133 offset:22528
	ds_read_b128 v[194:197], v133 offset:23552
	buffer_load_dwordx4 v130, s[4:7], s45 offen lds
	s_add_i32 s47, s45, 0x20000
	s_mov_b32 m0, s14
	s_nop 0
	buffer_load_dwordx4 v130, s[4:7], s47 offen lds
	s_add_i32 s47, s45, 0x40000
	s_mov_b32 m0, s15
	s_nop 0
	buffer_load_dwordx4 v130, s[4:7], s47 offen lds
	s_add_i32 s47, s45, 0x60000
	s_mov_b32 m0, s16
	s_nop 0
	buffer_load_dwordx4 v130, s[4:7], s47 offen lds
	s_mov_b32 m0, s12
	s_add_i32 s47, s44, 0x20000
	buffer_load_dwordx4 v129, s[60:63], s44 offen lds
	s_mov_b32 m0, s17
	s_nop 0
	buffer_load_dwordx4 v129, s[60:63], s47 offen lds
	s_waitcnt vmcnt(8)
	s_waitcnt lgkmcnt(0)
	s_barrier
	s_setprio 1
	s_waitcnt lgkmcnt(0)
	v_mfma_f32_16x16x32_bf16 v[60:63], v[134:137], v[166:169], v[60:63]
	v_mfma_f32_16x16x32_bf16 v[56:59], v[142:145], v[166:169], v[56:59]
	s_waitcnt lgkmcnt(5)
	v_mfma_f32_16x16x32_bf16 v[52:55], v[134:137], v[174:177], v[52:55]
	v_mfma_f32_16x16x32_bf16 v[48:51], v[142:145], v[174:177], v[48:51]
	s_waitcnt lgkmcnt(3)
	v_mfma_f32_16x16x32_bf16 v[36:39], v[134:137], v[182:185], v[36:39]
	v_mfma_f32_16x16x32_bf16 v[32:35], v[142:145], v[182:185], v[32:35]
	s_waitcnt lgkmcnt(1)
	v_mfma_f32_16x16x32_bf16 v[20:23], v[134:137], v[190:193], v[20:23]
	v_mfma_f32_16x16x32_bf16 v[16:19], v[142:145], v[190:193], v[16:19]
	v_mfma_f32_16x16x32_bf16 v[60:63], v[138:141], v[170:173], v[60:63]
	v_mfma_f32_16x16x32_bf16 v[56:59], v[146:149], v[170:173], v[56:59]
	v_mfma_f32_16x16x32_bf16 v[52:55], v[138:141], v[178:181], v[52:55]
	v_mfma_f32_16x16x32_bf16 v[48:51], v[146:149], v[178:181], v[48:51]
	v_mfma_f32_16x16x32_bf16 v[36:39], v[138:141], v[186:189], v[36:39]
	v_mfma_f32_16x16x32_bf16 v[32:35], v[146:149], v[186:189], v[32:35]
	s_waitcnt lgkmcnt(0)
	v_mfma_f32_16x16x32_bf16 v[20:23], v[138:141], v[194:197], v[20:23]
	v_mfma_f32_16x16x32_bf16 v[16:19], v[146:149], v[194:197], v[16:19]
	s_setprio 0
	s_setprio 1
	v_mfma_f32_16x16x32_bf16 v[44:47], v[150:153], v[166:169], v[44:47]
	v_mfma_f32_16x16x32_bf16 v[40:43], v[158:161], v[166:169], v[40:43]
	v_mfma_f32_16x16x32_bf16 v[28:31], v[150:153], v[174:177], v[28:31]
	v_mfma_f32_16x16x32_bf16 v[24:27], v[158:161], v[174:177], v[24:27]
	v_mfma_f32_16x16x32_bf16 v[12:15], v[150:153], v[182:185], v[12:15]
	v_mfma_f32_16x16x32_bf16 v[8:11], v[158:161], v[182:185], v[8:11]
	v_mfma_f32_16x16x32_bf16 v[4:7], v[150:153], v[190:193], v[4:7]
	v_mfma_f32_16x16x32_bf16 v[0:3], v[158:161], v[190:193], v[0:3]
	v_mfma_f32_16x16x32_bf16 v[44:47], v[154:157], v[170:173], v[44:47]
	v_mfma_f32_16x16x32_bf16 v[40:43], v[162:165], v[170:173], v[40:43]
	v_mfma_f32_16x16x32_bf16 v[28:31], v[154:157], v[178:181], v[28:31]
	v_mfma_f32_16x16x32_bf16 v[24:27], v[162:165], v[178:181], v[24:27]
	v_mfma_f32_16x16x32_bf16 v[12:15], v[154:157], v[186:189], v[12:15]
	v_mfma_f32_16x16x32_bf16 v[8:11], v[162:165], v[186:189], v[8:11]
	v_mfma_f32_16x16x32_bf16 v[4:7], v[154:157], v[194:197], v[4:7]
	v_mfma_f32_16x16x32_bf16 v[0:3], v[162:165], v[194:197], v[0:3]
	s_setprio 0
	s_barrier
	ds_read_b128 v[134:137], v132 offset:32768
	ds_read_b128 v[138:141], v132 offset:33792
	ds_read_b128 v[142:145], v132 offset:34816
	ds_read_b128 v[146:149], v132 offset:35840
	ds_read_b128 v[150:153], v132 offset:49152
	ds_read_b128 v[154:157], v132 offset:50176
	ds_read_b128 v[158:161], v132 offset:51200
	ds_read_b128 v[162:165], v132 offset:52224
	s_mov_b32 m0, s18
	s_add_i32 s47, s44, 0x40000
	ds_read_b128 v[166:169], v133 offset:32768
	ds_read_b128 v[170:173], v133 offset:33792
	ds_read_b128 v[174:177], v133 offset:34816
	ds_read_b128 v[178:181], v133 offset:35840
	ds_read_b128 v[182:185], v133 offset:36864
	ds_read_b128 v[186:189], v133 offset:37888
	ds_read_b128 v[190:193], v133 offset:38912
	ds_read_b128 v[194:197], v133 offset:39936
	buffer_load_dwordx4 v129, s[60:63], s47 offen lds
	s_add_i32 s47, s44, 0x60000
	s_mov_b32 m0, s19
	s_nop 0
	buffer_load_dwordx4 v129, s[60:63], s47 offen lds
	s_waitcnt vmcnt(8)
	s_waitcnt lgkmcnt(0)
	s_barrier
	s_setprio 1
	s_waitcnt lgkmcnt(0)
	v_mfma_f32_16x16x32_bf16 v[124:127], v[134:137], v[166:169], v[124:127]
	v_mfma_f32_16x16x32_bf16 v[120:123], v[142:145], v[166:169], v[120:123]
	s_waitcnt lgkmcnt(5)
	v_mfma_f32_16x16x32_bf16 v[116:119], v[134:137], v[174:177], v[116:119]
	v_mfma_f32_16x16x32_bf16 v[112:115], v[142:145], v[174:177], v[112:115]
	s_waitcnt lgkmcnt(3)
	v_mfma_f32_16x16x32_bf16 v[100:103], v[134:137], v[182:185], v[100:103]
	v_mfma_f32_16x16x32_bf16 v[96:99], v[142:145], v[182:185], v[96:99]
	s_waitcnt lgkmcnt(1)
	v_mfma_f32_16x16x32_bf16 v[84:87], v[134:137], v[190:193], v[84:87]
	v_mfma_f32_16x16x32_bf16 v[80:83], v[142:145], v[190:193], v[80:83]
	v_mfma_f32_16x16x32_bf16 v[124:127], v[138:141], v[170:173], v[124:127]
	v_mfma_f32_16x16x32_bf16 v[120:123], v[146:149], v[170:173], v[120:123]
	v_mfma_f32_16x16x32_bf16 v[116:119], v[138:141], v[178:181], v[116:119]
	v_mfma_f32_16x16x32_bf16 v[112:115], v[146:149], v[178:181], v[112:115]
	v_mfma_f32_16x16x32_bf16 v[100:103], v[138:141], v[186:189], v[100:103]
	v_mfma_f32_16x16x32_bf16 v[96:99], v[146:149], v[186:189], v[96:99]
	s_waitcnt lgkmcnt(0)
	v_mfma_f32_16x16x32_bf16 v[84:87], v[138:141], v[194:197], v[84:87]
	v_mfma_f32_16x16x32_bf16 v[80:83], v[146:149], v[194:197], v[80:83]
	s_setprio 0
	s_setprio 1
	v_mfma_f32_16x16x32_bf16 v[108:111], v[150:153], v[166:169], v[108:111]
	v_mfma_f32_16x16x32_bf16 v[104:107], v[158:161], v[166:169], v[104:107]
	v_mfma_f32_16x16x32_bf16 v[92:95], v[150:153], v[174:177], v[92:95]
	v_mfma_f32_16x16x32_bf16 v[88:91], v[158:161], v[174:177], v[88:91]
	v_mfma_f32_16x16x32_bf16 v[76:79], v[150:153], v[182:185], v[76:79]
	v_mfma_f32_16x16x32_bf16 v[72:75], v[158:161], v[182:185], v[72:75]
	v_mfma_f32_16x16x32_bf16 v[68:71], v[150:153], v[190:193], v[68:71]
	v_mfma_f32_16x16x32_bf16 v[64:67], v[158:161], v[190:193], v[64:67]
	v_mfma_f32_16x16x32_bf16 v[108:111], v[154:157], v[170:173], v[108:111]
	v_mfma_f32_16x16x32_bf16 v[104:107], v[162:165], v[170:173], v[104:107]
	v_mfma_f32_16x16x32_bf16 v[92:95], v[154:157], v[178:181], v[92:95]
	v_mfma_f32_16x16x32_bf16 v[88:91], v[162:165], v[178:181], v[88:91]
	v_mfma_f32_16x16x32_bf16 v[76:79], v[154:157], v[186:189], v[76:79]
	v_mfma_f32_16x16x32_bf16 v[72:75], v[162:165], v[186:189], v[72:75]
	v_mfma_f32_16x16x32_bf16 v[68:71], v[154:157], v[194:197], v[68:71]
	v_mfma_f32_16x16x32_bf16 v[64:67], v[162:165], v[194:197], v[64:67]
	s_setprio 0
	s_barrier
	s_mov_b32 m0, s20
	ds_read_b128 v[166:169], v133 offset:49152
	ds_read_b128 v[170:173], v133 offset:50176
	ds_read_b128 v[174:177], v133 offset:51200
	ds_read_b128 v[178:181], v133 offset:52224
	ds_read_b128 v[182:185], v133 offset:53248
	ds_read_b128 v[186:189], v133 offset:54272
	ds_read_b128 v[190:193], v133 offset:55296
	ds_read_b128 v[194:197], v133 offset:56320
	buffer_load_dwordx4 v130, s[4:7], s46 offen lds
	s_add_i32 s46, s45, 0x20080
	s_mov_b32 m0, s21
	s_or_b32 s47, s44, 0x80
	buffer_load_dwordx4 v130, s[4:7], s46 offen lds
	s_add_i32 s46, s45, 0x40080
	s_mov_b32 m0, s24
	s_add_i32 s45, s45, 0x60080
	buffer_load_dwordx4 v130, s[4:7], s46 offen lds
	s_mov_b32 m0, s25
	s_add_i32 s44, s44, 0x20080
	buffer_load_dwordx4 v130, s[4:7], s45 offen lds
	s_mov_b32 m0, s22
	s_nop 0
	buffer_load_dwordx4 v129, s[60:63], s47 offen lds
	s_mov_b32 m0, s23
	s_nop 0
	buffer_load_dwordx4 v129, s[60:63], s44 offen lds
	s_waitcnt vmcnt(8)
	s_waitcnt lgkmcnt(0)
	s_barrier
	s_setprio 1
	s_waitcnt lgkmcnt(0)
	v_mfma_f32_16x16x32_bf16 v[60:63], v[134:137], v[166:169], v[60:63]
	v_mfma_f32_16x16x32_bf16 v[56:59], v[142:145], v[166:169], v[56:59]
	s_waitcnt lgkmcnt(5)
	v_mfma_f32_16x16x32_bf16 v[52:55], v[134:137], v[174:177], v[52:55]
	v_mfma_f32_16x16x32_bf16 v[48:51], v[142:145], v[174:177], v[48:51]
	s_waitcnt lgkmcnt(3)
	v_mfma_f32_16x16x32_bf16 v[36:39], v[134:137], v[182:185], v[36:39]
	v_mfma_f32_16x16x32_bf16 v[32:35], v[142:145], v[182:185], v[32:35]
	s_waitcnt lgkmcnt(1)
	v_mfma_f32_16x16x32_bf16 v[20:23], v[134:137], v[190:193], v[20:23]
	v_mfma_f32_16x16x32_bf16 v[16:19], v[142:145], v[190:193], v[16:19]
	v_mfma_f32_16x16x32_bf16 v[60:63], v[138:141], v[170:173], v[60:63]
	v_mfma_f32_16x16x32_bf16 v[56:59], v[146:149], v[170:173], v[56:59]
	v_mfma_f32_16x16x32_bf16 v[52:55], v[138:141], v[178:181], v[52:55]
	v_mfma_f32_16x16x32_bf16 v[48:51], v[146:149], v[178:181], v[48:51]
	v_mfma_f32_16x16x32_bf16 v[36:39], v[138:141], v[186:189], v[36:39]
	v_mfma_f32_16x16x32_bf16 v[32:35], v[146:149], v[186:189], v[32:35]
	s_waitcnt lgkmcnt(0)
	v_mfma_f32_16x16x32_bf16 v[20:23], v[138:141], v[194:197], v[20:23]
	v_mfma_f32_16x16x32_bf16 v[16:19], v[146:149], v[194:197], v[16:19]
	s_setprio 0
	s_setprio 1
	v_mfma_f32_16x16x32_bf16 v[44:47], v[150:153], v[166:169], v[44:47]
	v_mfma_f32_16x16x32_bf16 v[40:43], v[158:161], v[166:169], v[40:43]
	v_mfma_f32_16x16x32_bf16 v[28:31], v[150:153], v[174:177], v[28:31]
	v_mfma_f32_16x16x32_bf16 v[24:27], v[158:161], v[174:177], v[24:27]
	v_mfma_f32_16x16x32_bf16 v[12:15], v[150:153], v[182:185], v[12:15]
	v_mfma_f32_16x16x32_bf16 v[8:11], v[158:161], v[182:185], v[8:11]
	v_mfma_f32_16x16x32_bf16 v[4:7], v[150:153], v[190:193], v[4:7]
	v_mfma_f32_16x16x32_bf16 v[0:3], v[158:161], v[190:193], v[0:3]
	v_mfma_f32_16x16x32_bf16 v[44:47], v[154:157], v[170:173], v[44:47]
	v_mfma_f32_16x16x32_bf16 v[40:43], v[162:165], v[170:173], v[40:43]
	v_mfma_f32_16x16x32_bf16 v[28:31], v[154:157], v[178:181], v[28:31]
	v_mfma_f32_16x16x32_bf16 v[24:27], v[162:165], v[178:181], v[24:27]
	v_mfma_f32_16x16x32_bf16 v[12:15], v[154:157], v[186:189], v[12:15]
	v_mfma_f32_16x16x32_bf16 v[8:11], v[162:165], v[186:189], v[8:11]
	v_mfma_f32_16x16x32_bf16 v[4:7], v[154:157], v[194:197], v[4:7]
	v_mfma_f32_16x16x32_bf16 v[0:3], v[162:165], v[194:197], v[0:3]
	s_add_i32 s43, s43, 2
	s_addk_i32 s41, 0x100
	s_addk_i32 s42, 0x100
	s_cmp_gt_u32 s43, 13
	s_setprio 0
	s_barrier
	s_cbranch_scc0 .LBB0_426
	s_and_b64 vcc, exec, s[10:11]
	s_cbranch_vccz .LBB0_429
	s_barrier

.LBB0_1161:
	ds_read_b128 v[128:131], v151
	ds_read_b128 v[132:135], v151 offset:1024
	ds_read_b128 v[136:139], v151 offset:2048
	ds_read_b128 v[140:143], v151 offset:3072
	ds_read_b128 v[144:147], v151 offset:16384
	ds_read_b128 v[154:157], v151 offset:17408
	ds_read_b128 v[158:161], v151 offset:18432
	ds_read_b128 v[162:165], v151 offset:19456
	s_add_i32 s10, s58, 0xfffa0080
	s_cmp_eq_u32 s60, 12
	s_cselect_b32 s64, s56, s59
	s_cselect_b32 s61, s57, s10
	s_or_b32 s66, s64, 0x80
	s_add_i32 s10, s58, 0xfffe0000
	s_mov_b32 m0, s46
	ds_read_b128 v[166:169], v152
	ds_read_b128 v[170:173], v152 offset:1024
	ds_read_b128 v[174:177], v152 offset:2048
	ds_read_b128 v[178:181], v152 offset:3072
	ds_read_b128 v[182:185], v152 offset:4096
	ds_read_b128 v[186:189], v152 offset:5120
	ds_read_b128 v[190:193], v152 offset:6144
	ds_read_b128 v[194:197], v152 offset:7168
	buffer_load_dwordx4 v149, s[4:7], s10 offen lds
	s_mov_b32 m0, s47
	s_nop 0
	buffer_load_dwordx4 v149, s[4:7], s58 offen lds
	s_waitcnt vmcnt(8)
	s_waitcnt lgkmcnt(0)
	s_barrier
	s_setprio 1
	s_waitcnt lgkmcnt(7)
	v_mfma_f32_16x16x32_bf16 v[124:127], v[128:131], v[166:169], v[124:127]
	v_mfma_f32_16x16x32_bf16 v[120:123], v[136:139], v[166:169], v[120:123]
	s_waitcnt lgkmcnt(5)
	v_mfma_f32_16x16x32_bf16 v[108:111], v[128:131], v[174:177], v[108:111]
	v_mfma_f32_16x16x32_bf16 v[104:107], v[136:139], v[174:177], v[104:107]
	s_waitcnt lgkmcnt(3)
	v_mfma_f32_16x16x32_bf16 v[92:95], v[128:131], v[182:185], v[92:95]
	v_mfma_f32_16x16x32_bf16 v[88:91], v[136:139], v[182:185], v[88:91]
	s_waitcnt lgkmcnt(1)
	v_mfma_f32_16x16x32_bf16 v[76:79], v[128:131], v[190:193], v[76:79]
	v_mfma_f32_16x16x32_bf16 v[72:75], v[136:139], v[190:193], v[72:75]
	v_mfma_f32_16x16x32_bf16 v[124:127], v[132:135], v[170:173], v[124:127]
	v_mfma_f32_16x16x32_bf16 v[120:123], v[140:143], v[170:173], v[120:123]
	v_mfma_f32_16x16x32_bf16 v[108:111], v[132:135], v[178:181], v[108:111]
	v_mfma_f32_16x16x32_bf16 v[104:107], v[140:143], v[178:181], v[104:107]
	v_mfma_f32_16x16x32_bf16 v[92:95], v[132:135], v[186:189], v[92:95]
	v_mfma_f32_16x16x32_bf16 v[88:91], v[140:143], v[186:189], v[88:91]
	s_waitcnt lgkmcnt(0)
	v_mfma_f32_16x16x32_bf16 v[76:79], v[132:135], v[194:197], v[76:79]
	v_mfma_f32_16x16x32_bf16 v[72:75], v[140:143], v[194:197], v[72:75]
	s_setprio 0
	s_setprio 1
	v_mfma_f32_16x16x32_bf16 v[116:119], v[144:147], v[166:169], v[116:119]
	v_mfma_f32_16x16x32_bf16 v[112:115], v[158:161], v[166:169], v[112:115]
	v_mfma_f32_16x16x32_bf16 v[100:103], v[144:147], v[174:177], v[100:103]
	v_mfma_f32_16x16x32_bf16 v[96:99], v[158:161], v[174:177], v[96:99]
	v_mfma_f32_16x16x32_bf16 v[84:87], v[144:147], v[182:185], v[84:87]
	v_mfma_f32_16x16x32_bf16 v[80:83], v[158:161], v[182:185], v[80:83]
	v_mfma_f32_16x16x32_bf16 v[68:71], v[144:147], v[190:193], v[68:71]
	v_mfma_f32_16x16x32_bf16 v[64:67], v[158:161], v[190:193], v[64:67]
	v_mfma_f32_16x16x32_bf16 v[116:119], v[154:157], v[170:173], v[116:119]
	v_mfma_f32_16x16x32_bf16 v[112:115], v[162:165], v[170:173], v[112:115]
	v_mfma_f32_16x16x32_bf16 v[100:103], v[154:157], v[178:181], v[100:103]
	v_mfma_f32_16x16x32_bf16 v[96:99], v[162:165], v[178:181], v[96:99]
	v_mfma_f32_16x16x32_bf16 v[84:87], v[154:157], v[186:189], v[84:87]
	v_mfma_f32_16x16x32_bf16 v[80:83], v[162:165], v[186:189], v[80:83]
	v_mfma_f32_16x16x32_bf16 v[68:71], v[154:157], v[194:197], v[68:71]
	v_mfma_f32_16x16x32_bf16 v[64:67], v[162:165], v[194:197], v[64:67]
	s_setprio 0
	s_barrier
	s_mov_b32 m0, s26
	s_mov_b32 s10, s6
	s_mov_b32 s11, s7
	ds_read_b128 v[166:169], v152 offset:16384
	ds_read_b128 v[170:173], v152 offset:17408
	ds_read_b128 v[174:177], v152 offset:18432
	ds_read_b128 v[178:181], v152 offset:19456
	ds_read_b128 v[182:185], v152 offset:20480
	ds_read_b128 v[186:189], v152 offset:21504
	ds_read_b128 v[190:193], v152 offset:22528
	ds_read_b128 v[194:197], v152 offset:23552
	buffer_load_dwordx4 v149, s[8:11], s64 offen lds
	s_add_i32 s67, s64, 0x20000
	s_mov_b32 m0, s27
	s_nop 0
	buffer_load_dwordx4 v149, s[8:11], s67 offen lds
	s_add_i32 s67, s64, 0x40000
	s_mov_b32 m0, s28
	s_nop 0
	buffer_load_dwordx4 v149, s[8:11], s67 offen lds
	s_add_i32 s67, s64, 0x60000
	s_mov_b32 m0, s29
	s_nop 0
	buffer_load_dwordx4 v149, s[8:11], s67 offen lds
	s_mov_b32 m0, s25
	s_add_i32 s67, s61, 0x20000
	buffer_load_dwordx4 v149, s[4:7], s61 offen lds
	s_mov_b32 m0, s31
	s_nop 0
	buffer_load_dwordx4 v149, s[4:7], s67 offen lds
	s_waitcnt vmcnt(8)
	s_waitcnt lgkmcnt(0)
	s_barrier
	s_setprio 1
	s_waitcnt lgkmcnt(7)
	v_mfma_f32_16x16x32_bf16 v[60:63], v[128:131], v[166:169], v[60:63]
	v_mfma_f32_16x16x32_bf16 v[56:59], v[136:139], v[166:169], v[56:59]
	s_waitcnt lgkmcnt(5)
	v_mfma_f32_16x16x32_bf16 v[44:47], v[128:131], v[174:177], v[44:47]
	v_mfma_f32_16x16x32_bf16 v[40:43], v[136:139], v[174:177], v[40:43]
	s_waitcnt lgkmcnt(3)
	v_mfma_f32_16x16x32_bf16 v[28:31], v[128:131], v[182:185], v[28:31]
	v_mfma_f32_16x16x32_bf16 v[24:27], v[136:139], v[182:185], v[24:27]
	s_waitcnt lgkmcnt(1)
	v_mfma_f32_16x16x32_bf16 v[12:15], v[128:131], v[190:193], v[12:15]
	v_mfma_f32_16x16x32_bf16 v[8:11], v[136:139], v[190:193], v[8:11]
	v_mfma_f32_16x16x32_bf16 v[60:63], v[132:135], v[170:173], v[60:63]
	v_mfma_f32_16x16x32_bf16 v[56:59], v[140:143], v[170:173], v[56:59]
	v_mfma_f32_16x16x32_bf16 v[44:47], v[132:135], v[178:181], v[44:47]
	v_mfma_f32_16x16x32_bf16 v[40:43], v[140:143], v[178:181], v[40:43]
	v_mfma_f32_16x16x32_bf16 v[28:31], v[132:135], v[186:189], v[28:31]
	v_mfma_f32_16x16x32_bf16 v[24:27], v[140:143], v[186:189], v[24:27]
	s_waitcnt lgkmcnt(0)
	v_mfma_f32_16x16x32_bf16 v[12:15], v[132:135], v[194:197], v[12:15]
	v_mfma_f32_16x16x32_bf16 v[8:11], v[140:143], v[194:197], v[8:11]
	s_setprio 0
	s_setprio 1
	v_mfma_f32_16x16x32_bf16 v[52:55], v[144:147], v[166:169], v[52:55]
	v_mfma_f32_16x16x32_bf16 v[48:51], v[158:161], v[166:169], v[48:51]
	v_mfma_f32_16x16x32_bf16 v[36:39], v[144:147], v[174:177], v[36:39]
	v_mfma_f32_16x16x32_bf16 v[32:35], v[158:161], v[174:177], v[32:35]
	v_mfma_f32_16x16x32_bf16 v[20:23], v[144:147], v[182:185], v[20:23]
	v_mfma_f32_16x16x32_bf16 v[16:19], v[158:161], v[182:185], v[16:19]
	v_mfma_f32_16x16x32_bf16 v[4:7], v[144:147], v[190:193], v[4:7]
	v_mfma_f32_16x16x32_bf16 v[0:3], v[158:161], v[190:193], v[0:3]
	v_mfma_f32_16x16x32_bf16 v[52:55], v[154:157], v[170:173], v[52:55]
	v_mfma_f32_16x16x32_bf16 v[48:51], v[162:165], v[170:173], v[48:51]
	v_mfma_f32_16x16x32_bf16 v[36:39], v[154:157], v[178:181], v[36:39]
	v_mfma_f32_16x16x32_bf16 v[32:35], v[162:165], v[178:181], v[32:35]
	v_mfma_f32_16x16x32_bf16 v[20:23], v[154:157], v[186:189], v[20:23]
	v_mfma_f32_16x16x32_bf16 v[16:19], v[162:165], v[186:189], v[16:19]
	v_mfma_f32_16x16x32_bf16 v[4:7], v[154:157], v[194:197], v[4:7]
	v_mfma_f32_16x16x32_bf16 v[0:3], v[162:165], v[194:197], v[0:3]
	s_setprio 0
	s_barrier
	ds_read_b128 v[128:131], v151 offset:32768
	ds_read_b128 v[132:135], v151 offset:33792
	ds_read_b128 v[136:139], v151 offset:34816
	ds_read_b128 v[140:143], v151 offset:35840
	ds_read_b128 v[144:147], v151 offset:49152
	ds_read_b128 v[154:157], v151 offset:50176
	ds_read_b128 v[158:161], v151 offset:51200
	ds_read_b128 v[162:165], v151 offset:52224
	s_mov_b32 m0, s34
	s_add_i32 s67, s61, 0x40000
	ds_read_b128 v[166:169], v152 offset:32768
	ds_read_b128 v[170:173], v152 offset:33792
	ds_read_b128 v[174:177], v152 offset:34816
	ds_read_b128 v[178:181], v152 offset:35840
	ds_read_b128 v[182:185], v152 offset:36864
	ds_read_b128 v[186:189], v152 offset:37888
	ds_read_b128 v[190:193], v152 offset:38912
	ds_read_b128 v[194:197], v152 offset:39936
	buffer_load_dwordx4 v149, s[4:7], s67 offen lds
	s_add_i32 s67, s61, 0x60000
	s_mov_b32 m0, s35
	s_nop 0
	buffer_load_dwordx4 v149, s[4:7], s67 offen lds
	s_waitcnt vmcnt(8)
	s_waitcnt lgkmcnt(0)
	s_barrier
	s_setprio 1
	s_waitcnt lgkmcnt(7)
	v_mfma_f32_16x16x32_bf16 v[124:127], v[128:131], v[166:169], v[124:127]
	v_mfma_f32_16x16x32_bf16 v[120:123], v[136:139], v[166:169], v[120:123]
	s_waitcnt lgkmcnt(5)
	v_mfma_f32_16x16x32_bf16 v[108:111], v[128:131], v[174:177], v[108:111]
	v_mfma_f32_16x16x32_bf16 v[104:107], v[136:139], v[174:177], v[104:107]
	s_waitcnt lgkmcnt(3)
	v_mfma_f32_16x16x32_bf16 v[92:95], v[128:131], v[182:185], v[92:95]
	v_mfma_f32_16x16x32_bf16 v[88:91], v[136:139], v[182:185], v[88:91]
	s_waitcnt lgkmcnt(1)
	v_mfma_f32_16x16x32_bf16 v[76:79], v[128:131], v[190:193], v[76:79]
	v_mfma_f32_16x16x32_bf16 v[72:75], v[136:139], v[190:193], v[72:75]
	v_mfma_f32_16x16x32_bf16 v[124:127], v[132:135], v[170:173], v[124:127]
	v_mfma_f32_16x16x32_bf16 v[120:123], v[140:143], v[170:173], v[120:123]
	v_mfma_f32_16x16x32_bf16 v[108:111], v[132:135], v[178:181], v[108:111]
	v_mfma_f32_16x16x32_bf16 v[104:107], v[140:143], v[178:181], v[104:107]
	v_mfma_f32_16x16x32_bf16 v[92:95], v[132:135], v[186:189], v[92:95]
	v_mfma_f32_16x16x32_bf16 v[88:91], v[140:143], v[186:189], v[88:91]
	s_waitcnt lgkmcnt(0)
	v_mfma_f32_16x16x32_bf16 v[76:79], v[132:135], v[194:197], v[76:79]
	v_mfma_f32_16x16x32_bf16 v[72:75], v[140:143], v[194:197], v[72:75]
	s_setprio 0
	s_setprio 1
	v_mfma_f32_16x16x32_bf16 v[116:119], v[144:147], v[166:169], v[116:119]
	v_mfma_f32_16x16x32_bf16 v[112:115], v[158:161], v[166:169], v[112:115]
	v_mfma_f32_16x16x32_bf16 v[100:103], v[144:147], v[174:177], v[100:103]
	v_mfma_f32_16x16x32_bf16 v[96:99], v[158:161], v[174:177], v[96:99]
	v_mfma_f32_16x16x32_bf16 v[84:87], v[144:147], v[182:185], v[84:87]
	v_mfma_f32_16x16x32_bf16 v[80:83], v[158:161], v[182:185], v[80:83]
	v_mfma_f32_16x16x32_bf16 v[68:71], v[144:147], v[190:193], v[68:71]
	v_mfma_f32_16x16x32_bf16 v[64:67], v[158:161], v[190:193], v[64:67]
	v_mfma_f32_16x16x32_bf16 v[116:119], v[154:157], v[170:173], v[116:119]
	v_mfma_f32_16x16x32_bf16 v[112:115], v[162:165], v[170:173], v[112:115]
	v_mfma_f32_16x16x32_bf16 v[100:103], v[154:157], v[178:181], v[100:103]
	v_mfma_f32_16x16x32_bf16 v[96:99], v[162:165], v[178:181], v[96:99]
	v_mfma_f32_16x16x32_bf16 v[84:87], v[154:157], v[186:189], v[84:87]
	v_mfma_f32_16x16x32_bf16 v[80:83], v[162:165], v[186:189], v[80:83]
	v_mfma_f32_16x16x32_bf16 v[68:71], v[154:157], v[194:197], v[68:71]
	v_mfma_f32_16x16x32_bf16 v[64:67], v[162:165], v[194:197], v[64:67]
	s_setprio 0
	s_barrier
	s_mov_b32 m0, s38
	ds_read_b128 v[166:169], v152 offset:49152
	ds_read_b128 v[170:173], v152 offset:50176
	ds_read_b128 v[174:177], v152 offset:51200
	ds_read_b128 v[178:181], v152 offset:52224
	ds_read_b128 v[182:185], v152 offset:53248
	ds_read_b128 v[186:189], v152 offset:54272
	ds_read_b128 v[190:193], v152 offset:55296
	ds_read_b128 v[194:197], v152 offset:56320
	buffer_load_dwordx4 v149, s[8:11], s66 offen lds
	s_add_i32 s66, s64, 0x20080
	s_mov_b32 m0, s39
	s_or_b32 s67, s61, 0x80
	buffer_load_dwordx4 v149, s[8:11], s66 offen lds
	s_add_i32 s66, s64, 0x40080
	s_mov_b32 m0, s42
	s_add_i32 s64, s64, 0x60080
	buffer_load_dwordx4 v149, s[8:11], s66 offen lds
	s_mov_b32 m0, s43
	s_add_i32 s61, s61, 0x20080
	buffer_load_dwordx4 v149, s[8:11], s64 offen lds
	s_mov_b32 m0, s40
	s_nop 0
	buffer_load_dwordx4 v149, s[4:7], s67 offen lds
	s_mov_b32 m0, s41
	s_nop 0
	buffer_load_dwordx4 v149, s[4:7], s61 offen lds
	s_waitcnt vmcnt(8)
	s_waitcnt lgkmcnt(0)
	s_barrier
	s_setprio 1
	s_waitcnt lgkmcnt(7)
	v_mfma_f32_16x16x32_bf16 v[60:63], v[128:131], v[166:169], v[60:63]
	v_mfma_f32_16x16x32_bf16 v[56:59], v[136:139], v[166:169], v[56:59]
	s_waitcnt lgkmcnt(5)
	v_mfma_f32_16x16x32_bf16 v[44:47], v[128:131], v[174:177], v[44:47]
	v_mfma_f32_16x16x32_bf16 v[40:43], v[136:139], v[174:177], v[40:43]
	s_waitcnt lgkmcnt(3)
	v_mfma_f32_16x16x32_bf16 v[28:31], v[128:131], v[182:185], v[28:31]
	v_mfma_f32_16x16x32_bf16 v[24:27], v[136:139], v[182:185], v[24:27]
	s_waitcnt lgkmcnt(1)
	v_mfma_f32_16x16x32_bf16 v[12:15], v[128:131], v[190:193], v[12:15]
	v_mfma_f32_16x16x32_bf16 v[8:11], v[136:139], v[190:193], v[8:11]
	v_mfma_f32_16x16x32_bf16 v[60:63], v[132:135], v[170:173], v[60:63]
	v_mfma_f32_16x16x32_bf16 v[56:59], v[140:143], v[170:173], v[56:59]
	v_mfma_f32_16x16x32_bf16 v[44:47], v[132:135], v[178:181], v[44:47]
	v_mfma_f32_16x16x32_bf16 v[40:43], v[140:143], v[178:181], v[40:43]
	v_mfma_f32_16x16x32_bf16 v[28:31], v[132:135], v[186:189], v[28:31]
	v_mfma_f32_16x16x32_bf16 v[24:27], v[140:143], v[186:189], v[24:27]
	s_waitcnt lgkmcnt(0)
	v_mfma_f32_16x16x32_bf16 v[12:15], v[132:135], v[194:197], v[12:15]
	v_mfma_f32_16x16x32_bf16 v[8:11], v[140:143], v[194:197], v[8:11]
	s_setprio 0
	s_setprio 1
	v_mfma_f32_16x16x32_bf16 v[52:55], v[144:147], v[166:169], v[52:55]
	v_mfma_f32_16x16x32_bf16 v[48:51], v[158:161], v[166:169], v[48:51]
	v_mfma_f32_16x16x32_bf16 v[36:39], v[144:147], v[174:177], v[36:39]
	v_mfma_f32_16x16x32_bf16 v[32:35], v[158:161], v[174:177], v[32:35]
	v_mfma_f32_16x16x32_bf16 v[20:23], v[144:147], v[182:185], v[20:23]
	v_mfma_f32_16x16x32_bf16 v[16:19], v[158:161], v[182:185], v[16:19]
	v_mfma_f32_16x16x32_bf16 v[4:7], v[144:147], v[190:193], v[4:7]
	v_mfma_f32_16x16x32_bf16 v[0:3], v[158:161], v[190:193], v[0:3]
	v_mfma_f32_16x16x32_bf16 v[52:55], v[154:157], v[170:173], v[52:55]
	v_mfma_f32_16x16x32_bf16 v[48:51], v[162:165], v[170:173], v[48:51]
	v_mfma_f32_16x16x32_bf16 v[36:39], v[154:157], v[178:181], v[36:39]
	v_mfma_f32_16x16x32_bf16 v[32:35], v[162:165], v[178:181], v[32:35]
	v_mfma_f32_16x16x32_bf16 v[20:23], v[154:157], v[186:189], v[20:23]
	v_mfma_f32_16x16x32_bf16 v[16:19], v[162:165], v[186:189], v[16:19]
	v_mfma_f32_16x16x32_bf16 v[4:7], v[154:157], v[194:197], v[4:7]
	v_mfma_f32_16x16x32_bf16 v[0:3], v[162:165], v[194:197], v[0:3]
	s_add_i32 s60, s60, 2
	s_addk_i32 s58, 0x100
	s_addk_i32 s59, 0x100
	s_cmp_gt_u32 s60, 13
	s_setprio 0
	s_barrier
	s_cbranch_scc0 .LBB0_1161
	s_and_b64 vcc, exec, s[22:23]
	s_cbranch_vccz .LBB0_1164
	s_barrier

.LBB0_1183:
	ds_read_b128 v[128:131], v208
	ds_read_b128 v[132:135], v208 offset:1024
	ds_read_b128 v[136:139], v208 offset:2048
	ds_read_b128 v[140:143], v208 offset:3072
	ds_read_b128 v[144:147], v208 offset:16384
	ds_read_b128 v[148:151], v208 offset:17408
	ds_read_b128 v[152:155], v208 offset:18432
	ds_read_b128 v[156:159], v208 offset:19456
	s_add_i32 s10, s30, 0xfffa0080
	s_cmp_eq_u32 s34, 12
	s_cselect_b32 s36, s2, s31
	s_cselect_b32 s35, s3, s10
	s_or_b32 s37, s36, 0x80
	s_add_i32 s10, s30, 0xfffe0000
	s_mov_b32 m0, s57
	ds_read_b128 v[160:163], v246
	ds_read_b128 v[164:167], v246 offset:1024
	ds_read_b128 v[168:171], v246 offset:2048
	ds_read_b128 v[172:175], v246 offset:3072
	ds_read_b128 v[176:179], v246 offset:4096
	ds_read_b128 v[180:183], v246 offset:5120
	ds_read_b128 v[184:187], v246 offset:6144
	ds_read_b128 v[188:191], v246 offset:7168
	buffer_load_dwordx4 v244, s[4:7], s10 offen lds
	s_mov_b32 m0, s58
	s_nop 0
	buffer_load_dwordx4 v244, s[4:7], s30 offen lds
	s_waitcnt vmcnt(8)
	s_waitcnt lgkmcnt(0)
	s_barrier
	s_setprio 1
	s_waitcnt lgkmcnt(0)
	v_mfma_f32_16x16x32_bf16 v[72:75], v[128:131], v[160:163], v[72:75]
	v_mfma_f32_16x16x32_bf16 v[80:83], v[136:139], v[160:163], v[80:83]
	s_waitcnt lgkmcnt(5)
	v_mfma_f32_16x16x32_bf16 v[104:107], v[128:131], v[168:171], v[104:107]
	v_mfma_f32_16x16x32_bf16 v[108:111], v[136:139], v[168:171], v[108:111]
	s_waitcnt lgkmcnt(3)
	v_mfma_f32_16x16x32_bf16 v[120:123], v[128:131], v[176:179], v[120:123]
	v_mfma_f32_16x16x32_bf16 v[112:115], v[136:139], v[176:179], v[112:115]
	s_waitcnt lgkmcnt(1)
	v_mfma_f32_16x16x32_bf16 v[84:87], v[128:131], v[184:187], v[84:87]
	v_mfma_f32_16x16x32_bf16 v[76:79], v[136:139], v[184:187], v[76:79]
	v_mfma_f32_16x16x32_bf16 v[72:75], v[132:135], v[164:167], v[72:75]
	v_mfma_f32_16x16x32_bf16 v[80:83], v[140:143], v[164:167], v[80:83]
	v_mfma_f32_16x16x32_bf16 v[104:107], v[132:135], v[172:175], v[104:107]
	v_mfma_f32_16x16x32_bf16 v[108:111], v[140:143], v[172:175], v[108:111]
	v_mfma_f32_16x16x32_bf16 v[120:123], v[132:135], v[180:183], v[120:123]
	v_mfma_f32_16x16x32_bf16 v[112:115], v[140:143], v[180:183], v[112:115]
	s_waitcnt lgkmcnt(0)
	v_mfma_f32_16x16x32_bf16 v[84:87], v[132:135], v[188:191], v[84:87]
	v_mfma_f32_16x16x32_bf16 v[76:79], v[140:143], v[188:191], v[76:79]
	s_setprio 0
	s_setprio 1
	v_mfma_f32_16x16x32_bf16 v[88:91], v[144:147], v[160:163], v[88:91]
	v_mfma_f32_16x16x32_bf16 v[96:99], v[152:155], v[160:163], v[96:99]
	v_mfma_f32_16x16x32_bf16 v[116:119], v[144:147], v[168:171], v[116:119]
	v_mfma_f32_16x16x32_bf16 v[124:127], v[152:155], v[168:171], v[124:127]
	v_mfma_f32_16x16x32_bf16 v[100:103], v[144:147], v[176:179], v[100:103]
	v_mfma_f32_16x16x32_bf16 v[92:95], v[152:155], v[176:179], v[92:95]
	v_mfma_f32_16x16x32_bf16 v[68:71], v[144:147], v[184:187], v[68:71]
	v_mfma_f32_16x16x32_bf16 v[64:67], v[152:155], v[184:187], v[64:67]
	v_mfma_f32_16x16x32_bf16 v[88:91], v[148:151], v[164:167], v[88:91]
	v_mfma_f32_16x16x32_bf16 v[96:99], v[156:159], v[164:167], v[96:99]
	v_mfma_f32_16x16x32_bf16 v[116:119], v[148:151], v[172:175], v[116:119]
	v_mfma_f32_16x16x32_bf16 v[124:127], v[156:159], v[172:175], v[124:127]
	v_mfma_f32_16x16x32_bf16 v[100:103], v[148:151], v[180:183], v[100:103]
	v_mfma_f32_16x16x32_bf16 v[92:95], v[156:159], v[180:183], v[92:95]
	v_mfma_f32_16x16x32_bf16 v[68:71], v[148:151], v[188:191], v[68:71]
	v_mfma_f32_16x16x32_bf16 v[64:67], v[156:159], v[188:191], v[64:67]
	s_setprio 0
	s_barrier
	s_mov_b32 m0, s41
	s_mov_b32 s10, s6
	s_mov_b32 s11, s7
	ds_read_b128 v[160:163], v246 offset:16384
	ds_read_b128 v[164:167], v246 offset:17408
	ds_read_b128 v[168:171], v246 offset:18432
	ds_read_b128 v[172:175], v246 offset:19456
	ds_read_b128 v[176:179], v246 offset:20480
	ds_read_b128 v[180:183], v246 offset:21504
	ds_read_b128 v[184:187], v246 offset:22528
	ds_read_b128 v[188:191], v246 offset:23552
	buffer_load_dwordx4 v244, s[8:11], s36 offen lds
	s_add_i32 s38, s36, 0x20000
	s_mov_b32 m0, s42
	s_nop 0
	buffer_load_dwordx4 v244, s[8:11], s38 offen lds
	s_add_i32 s38, s36, 0x40000
	s_mov_b32 m0, s43
	s_nop 0
	buffer_load_dwordx4 v244, s[8:11], s38 offen lds
	s_add_i32 s38, s36, 0x60000
	s_mov_b32 m0, s44
	s_nop 0
	buffer_load_dwordx4 v244, s[8:11], s38 offen lds
	s_mov_b32 m0, s40
	s_add_i32 s38, s35, 0x20000
	buffer_load_dwordx4 v244, s[4:7], s35 offen lds
	s_mov_b32 m0, s45
	s_nop 0
	buffer_load_dwordx4 v244, s[4:7], s38 offen lds
	s_waitcnt vmcnt(8)
	s_waitcnt lgkmcnt(0)
	s_barrier
	s_setprio 1
	s_waitcnt lgkmcnt(7)
	v_mfma_f32_16x16x32_bf16 v[60:63], v[128:131], v[160:163], v[60:63]
	v_mfma_f32_16x16x32_bf16 v[56:59], v[136:139], v[160:163], v[56:59]
	s_waitcnt lgkmcnt(5)
	v_mfma_f32_16x16x32_bf16 v[44:47], v[128:131], v[168:171], v[44:47]
	v_mfma_f32_16x16x32_bf16 v[40:43], v[136:139], v[168:171], v[40:43]
	s_waitcnt lgkmcnt(3)
	v_mfma_f32_16x16x32_bf16 v[28:31], v[128:131], v[176:179], v[28:31]
	v_mfma_f32_16x16x32_bf16 v[24:27], v[136:139], v[176:179], v[24:27]
	s_waitcnt lgkmcnt(1)
	v_mfma_f32_16x16x32_bf16 v[12:15], v[128:131], v[184:187], v[12:15]
	v_mfma_f32_16x16x32_bf16 v[8:11], v[136:139], v[184:187], v[8:11]
	v_mfma_f32_16x16x32_bf16 v[60:63], v[132:135], v[164:167], v[60:63]
	v_mfma_f32_16x16x32_bf16 v[56:59], v[140:143], v[164:167], v[56:59]
	v_mfma_f32_16x16x32_bf16 v[44:47], v[132:135], v[172:175], v[44:47]
	v_mfma_f32_16x16x32_bf16 v[40:43], v[140:143], v[172:175], v[40:43]
	v_mfma_f32_16x16x32_bf16 v[28:31], v[132:135], v[180:183], v[28:31]
	v_mfma_f32_16x16x32_bf16 v[24:27], v[140:143], v[180:183], v[24:27]
	s_waitcnt lgkmcnt(0)
	v_mfma_f32_16x16x32_bf16 v[12:15], v[132:135], v[188:191], v[12:15]
	v_mfma_f32_16x16x32_bf16 v[8:11], v[140:143], v[188:191], v[8:11]
	s_setprio 0
	s_setprio 1
	v_mfma_f32_16x16x32_bf16 v[52:55], v[144:147], v[160:163], v[52:55]
	v_mfma_f32_16x16x32_bf16 v[48:51], v[152:155], v[160:163], v[48:51]
	v_mfma_f32_16x16x32_bf16 v[36:39], v[144:147], v[168:171], v[36:39]
	v_mfma_f32_16x16x32_bf16 v[32:35], v[152:155], v[168:171], v[32:35]
	v_mfma_f32_16x16x32_bf16 v[20:23], v[144:147], v[176:179], v[20:23]
	v_mfma_f32_16x16x32_bf16 v[16:19], v[152:155], v[176:179], v[16:19]
	v_mfma_f32_16x16x32_bf16 v[4:7], v[144:147], v[184:187], v[4:7]
	v_mfma_f32_16x16x32_bf16 v[0:3], v[152:155], v[184:187], v[0:3]
	v_mfma_f32_16x16x32_bf16 v[52:55], v[148:151], v[164:167], v[52:55]
	v_mfma_f32_16x16x32_bf16 v[48:51], v[156:159], v[164:167], v[48:51]
	v_mfma_f32_16x16x32_bf16 v[36:39], v[148:151], v[172:175], v[36:39]
	v_mfma_f32_16x16x32_bf16 v[32:35], v[156:159], v[172:175], v[32:35]
	v_mfma_f32_16x16x32_bf16 v[20:23], v[148:151], v[180:183], v[20:23]
	v_mfma_f32_16x16x32_bf16 v[16:19], v[156:159], v[180:183], v[16:19]
	v_mfma_f32_16x16x32_bf16 v[4:7], v[148:151], v[188:191], v[4:7]
	v_mfma_f32_16x16x32_bf16 v[0:3], v[156:159], v[188:191], v[0:3]
	s_setprio 0
	s_barrier
	ds_read_b128 v[128:131], v208 offset:32768
	ds_read_b128 v[132:135], v208 offset:33792
	ds_read_b128 v[136:139], v208 offset:34816
	ds_read_b128 v[140:143], v208 offset:35840
	ds_read_b128 v[144:147], v208 offset:49152
	ds_read_b128 v[148:151], v208 offset:50176
	ds_read_b128 v[152:155], v208 offset:51200
	ds_read_b128 v[156:159], v208 offset:52224
	s_mov_b32 m0, s46
	s_add_i32 s38, s35, 0x40000
	ds_read_b128 v[160:163], v246 offset:32768
	ds_read_b128 v[164:167], v246 offset:33792
	ds_read_b128 v[168:171], v246 offset:34816
	ds_read_b128 v[172:175], v246 offset:35840
	ds_read_b128 v[176:179], v246 offset:36864
	ds_read_b128 v[180:183], v246 offset:37888
	ds_read_b128 v[184:187], v246 offset:38912
	ds_read_b128 v[188:191], v246 offset:39936
	buffer_load_dwordx4 v244, s[4:7], s38 offen lds
	s_add_i32 s38, s35, 0x60000
	s_mov_b32 m0, s47
	s_nop 0
	buffer_load_dwordx4 v244, s[4:7], s38 offen lds
	s_waitcnt vmcnt(8)
	s_waitcnt lgkmcnt(0)
	s_barrier
	s_setprio 1
	s_waitcnt lgkmcnt(7)
	v_mfma_f32_16x16x32_bf16 v[72:75], v[128:131], v[160:163], v[72:75]
	v_mfma_f32_16x16x32_bf16 v[80:83], v[136:139], v[160:163], v[80:83]
	s_waitcnt lgkmcnt(5)
	v_mfma_f32_16x16x32_bf16 v[104:107], v[128:131], v[168:171], v[104:107]
	v_mfma_f32_16x16x32_bf16 v[108:111], v[136:139], v[168:171], v[108:111]
	s_waitcnt lgkmcnt(3)
	v_mfma_f32_16x16x32_bf16 v[120:123], v[128:131], v[176:179], v[120:123]
	v_mfma_f32_16x16x32_bf16 v[112:115], v[136:139], v[176:179], v[112:115]
	s_waitcnt lgkmcnt(1)
	v_mfma_f32_16x16x32_bf16 v[84:87], v[128:131], v[184:187], v[84:87]
	v_mfma_f32_16x16x32_bf16 v[76:79], v[136:139], v[184:187], v[76:79]
	v_mfma_f32_16x16x32_bf16 v[72:75], v[132:135], v[164:167], v[72:75]
	v_mfma_f32_16x16x32_bf16 v[80:83], v[140:143], v[164:167], v[80:83]
	v_mfma_f32_16x16x32_bf16 v[104:107], v[132:135], v[172:175], v[104:107]
	v_mfma_f32_16x16x32_bf16 v[108:111], v[140:143], v[172:175], v[108:111]
	v_mfma_f32_16x16x32_bf16 v[120:123], v[132:135], v[180:183], v[120:123]
	v_mfma_f32_16x16x32_bf16 v[112:115], v[140:143], v[180:183], v[112:115]
	s_waitcnt lgkmcnt(0)
	v_mfma_f32_16x16x32_bf16 v[84:87], v[132:135], v[188:191], v[84:87]
	v_mfma_f32_16x16x32_bf16 v[76:79], v[140:143], v[188:191], v[76:79]
	s_setprio 0
	s_setprio 1
	v_mfma_f32_16x16x32_bf16 v[88:91], v[144:147], v[160:163], v[88:91]
	v_mfma_f32_16x16x32_bf16 v[96:99], v[152:155], v[160:163], v[96:99]
	v_mfma_f32_16x16x32_bf16 v[116:119], v[144:147], v[168:171], v[116:119]
	v_mfma_f32_16x16x32_bf16 v[124:127], v[152:155], v[168:171], v[124:127]
	v_mfma_f32_16x16x32_bf16 v[100:103], v[144:147], v[176:179], v[100:103]
	v_mfma_f32_16x16x32_bf16 v[92:95], v[152:155], v[176:179], v[92:95]
	v_mfma_f32_16x16x32_bf16 v[68:71], v[144:147], v[184:187], v[68:71]
	v_mfma_f32_16x16x32_bf16 v[64:67], v[152:155], v[184:187], v[64:67]
	v_mfma_f32_16x16x32_bf16 v[88:91], v[148:151], v[164:167], v[88:91]
	v_mfma_f32_16x16x32_bf16 v[96:99], v[156:159], v[164:167], v[96:99]
	v_mfma_f32_16x16x32_bf16 v[116:119], v[148:151], v[172:175], v[116:119]
	v_mfma_f32_16x16x32_bf16 v[124:127], v[156:159], v[172:175], v[124:127]
	v_mfma_f32_16x16x32_bf16 v[100:103], v[148:151], v[180:183], v[100:103]
	v_mfma_f32_16x16x32_bf16 v[92:95], v[156:159], v[180:183], v[92:95]
	v_mfma_f32_16x16x32_bf16 v[68:71], v[148:151], v[188:191], v[68:71]
	v_mfma_f32_16x16x32_bf16 v[64:67], v[156:159], v[188:191], v[64:67]
	s_setprio 0
	s_barrier
	s_mov_b32 m0, s48
	ds_read_b128 v[160:163], v246 offset:49152
	ds_read_b128 v[164:167], v246 offset:50176
	ds_read_b128 v[168:171], v246 offset:51200
	ds_read_b128 v[172:175], v246 offset:52224
	ds_read_b128 v[176:179], v246 offset:53248
	ds_read_b128 v[180:183], v246 offset:54272
	ds_read_b128 v[184:187], v246 offset:55296
	ds_read_b128 v[188:191], v246 offset:56320
	buffer_load_dwordx4 v244, s[8:11], s37 offen lds
	s_add_i32 s37, s36, 0x20080
	s_mov_b32 m0, s49
	s_or_b32 s38, s35, 0x80
	buffer_load_dwordx4 v244, s[8:11], s37 offen lds
	s_add_i32 s37, s36, 0x40080
	s_mov_b32 m0, s52
	s_add_i32 s36, s36, 0x60080
	buffer_load_dwordx4 v244, s[8:11], s37 offen lds
	s_mov_b32 m0, s53
	s_add_i32 s35, s35, 0x20080
	buffer_load_dwordx4 v244, s[8:11], s36 offen lds
	s_mov_b32 m0, s50
	s_nop 0
	buffer_load_dwordx4 v244, s[4:7], s38 offen lds
	s_mov_b32 m0, s51
	s_nop 0
	buffer_load_dwordx4 v244, s[4:7], s35 offen lds
	s_waitcnt vmcnt(8)
	s_waitcnt lgkmcnt(0)
	s_barrier
	s_setprio 1
	s_waitcnt lgkmcnt(7)
	v_mfma_f32_16x16x32_bf16 v[60:63], v[128:131], v[160:163], v[60:63]
	v_mfma_f32_16x16x32_bf16 v[56:59], v[136:139], v[160:163], v[56:59]
	s_waitcnt lgkmcnt(5)
	v_mfma_f32_16x16x32_bf16 v[44:47], v[128:131], v[168:171], v[44:47]
	v_mfma_f32_16x16x32_bf16 v[40:43], v[136:139], v[168:171], v[40:43]
	s_waitcnt lgkmcnt(3)
	v_mfma_f32_16x16x32_bf16 v[28:31], v[128:131], v[176:179], v[28:31]
	v_mfma_f32_16x16x32_bf16 v[24:27], v[136:139], v[176:179], v[24:27]
	s_waitcnt lgkmcnt(1)
	v_mfma_f32_16x16x32_bf16 v[12:15], v[128:131], v[184:187], v[12:15]
	v_mfma_f32_16x16x32_bf16 v[8:11], v[136:139], v[184:187], v[8:11]
	v_mfma_f32_16x16x32_bf16 v[60:63], v[132:135], v[164:167], v[60:63]
	v_mfma_f32_16x16x32_bf16 v[56:59], v[140:143], v[164:167], v[56:59]
	v_mfma_f32_16x16x32_bf16 v[44:47], v[132:135], v[172:175], v[44:47]
	v_mfma_f32_16x16x32_bf16 v[40:43], v[140:143], v[172:175], v[40:43]
	v_mfma_f32_16x16x32_bf16 v[28:31], v[132:135], v[180:183], v[28:31]
	v_mfma_f32_16x16x32_bf16 v[24:27], v[140:143], v[180:183], v[24:27]
	s_waitcnt lgkmcnt(0)
	v_mfma_f32_16x16x32_bf16 v[12:15], v[132:135], v[188:191], v[12:15]
	v_mfma_f32_16x16x32_bf16 v[8:11], v[140:143], v[188:191], v[8:11]
	s_setprio 0
	s_setprio 1
	v_mfma_f32_16x16x32_bf16 v[52:55], v[144:147], v[160:163], v[52:55]
	v_mfma_f32_16x16x32_bf16 v[48:51], v[152:155], v[160:163], v[48:51]
	v_mfma_f32_16x16x32_bf16 v[36:39], v[144:147], v[168:171], v[36:39]
	v_mfma_f32_16x16x32_bf16 v[32:35], v[152:155], v[168:171], v[32:35]
	v_mfma_f32_16x16x32_bf16 v[20:23], v[144:147], v[176:179], v[20:23]
	v_mfma_f32_16x16x32_bf16 v[16:19], v[152:155], v[176:179], v[16:19]
	v_mfma_f32_16x16x32_bf16 v[4:7], v[144:147], v[184:187], v[4:7]
	v_mfma_f32_16x16x32_bf16 v[0:3], v[152:155], v[184:187], v[0:3]
	v_mfma_f32_16x16x32_bf16 v[52:55], v[148:151], v[164:167], v[52:55]
	v_mfma_f32_16x16x32_bf16 v[48:51], v[156:159], v[164:167], v[48:51]
	v_mfma_f32_16x16x32_bf16 v[36:39], v[148:151], v[172:175], v[36:39]
	v_mfma_f32_16x16x32_bf16 v[32:35], v[156:159], v[172:175], v[32:35]
	v_mfma_f32_16x16x32_bf16 v[20:23], v[148:151], v[180:183], v[20:23]
	v_mfma_f32_16x16x32_bf16 v[16:19], v[156:159], v[180:183], v[16:19]
	v_mfma_f32_16x16x32_bf16 v[4:7], v[148:151], v[188:191], v[4:7]
	v_mfma_f32_16x16x32_bf16 v[0:3], v[156:159], v[188:191], v[0:3]
	s_add_i32 s34, s34, 2
	s_addk_i32 s30, 0x100
	s_addk_i32 s31, 0x100
	s_cmp_gt_u32 s34, 13
	s_setprio 0
	s_barrier
	s_cbranch_scc0 .LBB0_1183
	s_and_b64 vcc, exec, s[22:23]
	s_cbranch_vccz .LBB0_1186
	s_barrier

.LBB0_1441:
	s_addk_i32 s42, 0x100
	s_add_i32 s43, s42, s66
	s_and_b64 s[40:41], s[38:39], exec
	s_waitcnt vmcnt(8)
	s_cselect_b32 s41, s67, s43
	s_add_i32 s42, s42, s57
	s_waitcnt lgkmcnt(0)
	s_and_b64 s[38:39], s[38:39], exec
	s_cselect_b32 s40, s56, s42
	s_add_i32 s38, s41, 0x80
	s_add_i32 s39, s40, 0x80
	s_barrier
	s_setprio 1
	s_waitcnt lgkmcnt(6)
	v_mfma_scale_f32_16x16x128_f8f6f4 v[188:191], v[16:23], v[56:63], v[188:191], v238, v238 op_sel_hi:[0,0,0]
	v_mfma_scale_f32_16x16x128_f8f6f4 v[184:187], v[24:31], v[56:63], v[184:187], v238, v238 op_sel_hi:[0,0,0]
	s_waitcnt lgkmcnt(4)
	v_mfma_scale_f32_16x16x128_f8f6f4 v[180:183], v[16:23], v[48:55], v[180:183], v238, v238 op_sel_hi:[0,0,0]
	v_mfma_scale_f32_16x16x128_f8f6f4 v[176:179], v[24:31], v[48:55], v[176:179], v238, v238 op_sel_hi:[0,0,0]
	s_waitcnt lgkmcnt(2)
	v_mfma_scale_f32_16x16x128_f8f6f4 v[172:175], v[16:23], v[40:47], v[172:175], v238, v238 op_sel_hi:[0,0,0]
	v_mfma_scale_f32_16x16x128_f8f6f4 v[168:171], v[24:31], v[40:47], v[168:171], v238, v238 op_sel_hi:[0,0,0]
	s_waitcnt lgkmcnt(0)
	v_mfma_scale_f32_16x16x128_f8f6f4 v[164:167], v[16:23], v[32:39], v[164:167], v238, v238 op_sel_hi:[0,0,0]
	v_mfma_scale_f32_16x16x128_f8f6f4 v[160:163], v[24:31], v[32:39], v[160:163], v238, v238 op_sel_hi:[0,0,0]
	s_setprio 0
	s_setprio 1
	v_mfma_scale_f32_16x16x128_f8f6f4 v[156:159], v[0:7], v[56:63], v[156:159], v238, v238 op_sel_hi:[0,0,0]
	v_mfma_scale_f32_16x16x128_f8f6f4 v[152:155], v[8:15], v[56:63], v[152:155], v238, v238 op_sel_hi:[0,0,0]
	v_mfma_scale_f32_16x16x128_f8f6f4 v[148:151], v[0:7], v[48:55], v[148:151], v238, v238 op_sel_hi:[0,0,0]
	v_mfma_scale_f32_16x16x128_f8f6f4 v[144:147], v[8:15], v[48:55], v[144:147], v238, v238 op_sel_hi:[0,0,0]
	v_mfma_scale_f32_16x16x128_f8f6f4 v[140:143], v[0:7], v[40:47], v[140:143], v238, v238 op_sel_hi:[0,0,0]
	v_mfma_scale_f32_16x16x128_f8f6f4 v[136:139], v[8:15], v[40:47], v[136:139], v238, v238 op_sel_hi:[0,0,0]
	v_mfma_scale_f32_16x16x128_f8f6f4 v[132:135], v[0:7], v[32:39], v[132:135], v238, v238 op_sel_hi:[0,0,0]
	v_mfma_scale_f32_16x16x128_f8f6f4 v[128:131], v[8:15], v[32:39], v[128:131], v238, v238 op_sel_hi:[0,0,0]
	s_setprio 0
	s_barrier
	s_mov_b32 m0, s74
	s_lshl_b32 s42, s50, 6
	ds_read_b128 v[32:35], v200 offset:16384
	ds_read_b128 v[36:39], v200 offset:17408
	ds_read_b128 v[40:43], v200 offset:18432
	ds_read_b128 v[44:47], v200 offset:19456
	ds_read_b128 v[48:51], v200 offset:20480
	ds_read_b128 v[52:55], v200 offset:21504
	ds_read_b128 v[56:59], v200 offset:22528
	ds_read_b128 v[60:63], v200 offset:23552
	buffer_load_dwordx4 v194, s[60:63], s41 offen lds
	s_add_i32 s41, s42, s41
	s_mov_b32 m0, s75
	s_nop 0
	buffer_load_dwordx4 v194, s[60:63], s41 offen lds
	s_add_i32 s41, s41, s42
	s_mov_b32 m0, s76
	s_nop 0
	buffer_load_dwordx4 v194, s[60:63], s41 offen lds
	s_add_i32 s41, s41, s42
	s_mov_b32 m0, s77
	s_nop 0
	buffer_load_dwordx4 v194, s[60:63], s41 offen lds
	s_mov_b32 m0, s73
	s_nop 0
	buffer_load_dwordx4 v192, s[60:63], s40 offen lds
	s_add_i32 s40, s42, s40
	s_mov_b32 m0, s78
	s_nop 0
	buffer_load_dwordx4 v192, s[60:63], s40 offen lds
	s_waitcnt vmcnt(8)
	s_waitcnt lgkmcnt(0)
	s_barrier
	s_setprio 1
	s_waitcnt lgkmcnt(6)
	v_mfma_scale_f32_16x16x128_f8f6f4 v[124:127], v[16:23], v[32:39], v[124:127], v238, v238 op_sel_hi:[0,0,0]
	v_mfma_scale_f32_16x16x128_f8f6f4 v[120:123], v[24:31], v[32:39], v[120:123], v238, v238 op_sel_hi:[0,0,0]
	s_waitcnt lgkmcnt(4)
	v_mfma_scale_f32_16x16x128_f8f6f4 v[116:119], v[16:23], v[40:47], v[116:119], v238, v238 op_sel_hi:[0,0,0]
	v_mfma_scale_f32_16x16x128_f8f6f4 v[112:115], v[24:31], v[40:47], v[112:115], v238, v238 op_sel_hi:[0,0,0]
	s_waitcnt lgkmcnt(2)
	v_mfma_scale_f32_16x16x128_f8f6f4 v[108:111], v[16:23], v[48:55], v[108:111], v238, v238 op_sel_hi:[0,0,0]
	v_mfma_scale_f32_16x16x128_f8f6f4 v[104:107], v[24:31], v[48:55], v[104:107], v238, v238 op_sel_hi:[0,0,0]
	s_waitcnt lgkmcnt(0)
	v_mfma_scale_f32_16x16x128_f8f6f4 v[100:103], v[16:23], v[56:63], v[100:103], v238, v238 op_sel_hi:[0,0,0]
	v_mfma_scale_f32_16x16x128_f8f6f4 v[96:99], v[24:31], v[56:63], v[96:99], v238, v238 op_sel_hi:[0,0,0]
	s_setprio 0
	s_setprio 1
	v_mfma_scale_f32_16x16x128_f8f6f4 v[92:95], v[0:7], v[32:39], v[92:95], v238, v238 op_sel_hi:[0,0,0]
	v_mfma_scale_f32_16x16x128_f8f6f4 v[88:91], v[8:15], v[32:39], v[88:91], v238, v238 op_sel_hi:[0,0,0]
	v_mfma_scale_f32_16x16x128_f8f6f4 v[84:87], v[0:7], v[40:47], v[84:87], v238, v238 op_sel_hi:[0,0,0]
	v_mfma_scale_f32_16x16x128_f8f6f4 v[80:83], v[8:15], v[40:47], v[80:83], v238, v238 op_sel_hi:[0,0,0]
	v_mfma_scale_f32_16x16x128_f8f6f4 v[76:79], v[0:7], v[48:55], v[76:79], v238, v238 op_sel_hi:[0,0,0]
	v_mfma_scale_f32_16x16x128_f8f6f4 v[72:75], v[8:15], v[48:55], v[72:75], v238, v238 op_sel_hi:[0,0,0]
	v_mfma_scale_f32_16x16x128_f8f6f4 v[68:71], v[0:7], v[56:63], v[68:71], v238, v238 op_sel_hi:[0,0,0]
	v_mfma_scale_f32_16x16x128_f8f6f4 v[64:67], v[8:15], v[56:63], v[64:67], v238, v238 op_sel_hi:[0,0,0]
	s_setprio 0
	s_barrier
	ds_read_b128 v[0:3], v199 offset:32768
	ds_read_b128 v[4:7], v199 offset:33792
	ds_read_b128 v[8:11], v199 offset:34816
	ds_read_b128 v[12:15], v199 offset:35840
	ds_read_b128 v[16:19], v199 offset:49152
	ds_read_b128 v[20:23], v199 offset:50176
	ds_read_b128 v[24:27], v199 offset:51200
	ds_read_b128 v[28:31], v199 offset:52224
	s_mov_b32 m0, s79
	s_add_i32 s40, s40, s42
	ds_read_b128 v[32:35], v200 offset:32768
	ds_read_b128 v[36:39], v200 offset:33792
	ds_read_b128 v[40:43], v200 offset:34816
	ds_read_b128 v[44:47], v200 offset:35840
	ds_read_b128 v[48:51], v200 offset:36864
	ds_read_b128 v[52:55], v200 offset:37888
	ds_read_b128 v[56:59], v200 offset:38912
	ds_read_b128 v[60:63], v200 offset:39936
	buffer_load_dwordx4 v192, s[60:63], s40 offen lds
	s_add_i32 s40, s40, s42
	s_mov_b32 m0, s80
	s_nop 0
	buffer_load_dwordx4 v192, s[60:63], s40 offen lds
	s_waitcnt vmcnt(8)
	s_waitcnt lgkmcnt(0)
	s_barrier
	s_setprio 1
	s_waitcnt lgkmcnt(6)
	v_mfma_scale_f32_16x16x128_f8f6f4 v[188:191], v[0:7], v[32:39], v[188:191], v238, v238 op_sel_hi:[0,0,0]
	v_mfma_scale_f32_16x16x128_f8f6f4 v[184:187], v[8:15], v[32:39], v[184:187], v238, v238 op_sel_hi:[0,0,0]
	s_waitcnt lgkmcnt(4)
	v_mfma_scale_f32_16x16x128_f8f6f4 v[180:183], v[0:7], v[40:47], v[180:183], v238, v238 op_sel_hi:[0,0,0]
	v_mfma_scale_f32_16x16x128_f8f6f4 v[176:179], v[8:15], v[40:47], v[176:179], v238, v238 op_sel_hi:[0,0,0]
	s_waitcnt lgkmcnt(2)
	v_mfma_scale_f32_16x16x128_f8f6f4 v[172:175], v[0:7], v[48:55], v[172:175], v238, v238 op_sel_hi:[0,0,0]
	v_mfma_scale_f32_16x16x128_f8f6f4 v[168:171], v[8:15], v[48:55], v[168:171], v238, v238 op_sel_hi:[0,0,0]
	s_waitcnt lgkmcnt(0)
	v_mfma_scale_f32_16x16x128_f8f6f4 v[164:167], v[0:7], v[56:63], v[164:167], v238, v238 op_sel_hi:[0,0,0]
	v_mfma_scale_f32_16x16x128_f8f6f4 v[160:163], v[8:15], v[56:63], v[160:163], v238, v238 op_sel_hi:[0,0,0]
	s_setprio 0
	s_setprio 1
	v_mfma_scale_f32_16x16x128_f8f6f4 v[156:159], v[16:23], v[32:39], v[156:159], v238, v238 op_sel_hi:[0,0,0]
	v_mfma_scale_f32_16x16x128_f8f6f4 v[152:155], v[24:31], v[32:39], v[152:155], v238, v238 op_sel_hi:[0,0,0]
	v_mfma_scale_f32_16x16x128_f8f6f4 v[148:151], v[16:23], v[40:47], v[148:151], v238, v238 op_sel_hi:[0,0,0]
	v_mfma_scale_f32_16x16x128_f8f6f4 v[144:147], v[24:31], v[40:47], v[144:147], v238, v238 op_sel_hi:[0,0,0]
	v_mfma_scale_f32_16x16x128_f8f6f4 v[140:143], v[16:23], v[48:55], v[140:143], v238, v238 op_sel_hi:[0,0,0]
	v_mfma_scale_f32_16x16x128_f8f6f4 v[136:139], v[24:31], v[48:55], v[136:139], v238, v238 op_sel_hi:[0,0,0]
	v_mfma_scale_f32_16x16x128_f8f6f4 v[132:135], v[16:23], v[56:63], v[132:135], v238, v238 op_sel_hi:[0,0,0]
	v_mfma_scale_f32_16x16x128_f8f6f4 v[128:131], v[24:31], v[56:63], v[128:131], v238, v238 op_sel_hi:[0,0,0]
	s_setprio 0
	s_barrier
	s_mov_b32 m0, s83
	ds_read_b128 v[32:35], v200 offset:49152
	ds_read_b128 v[36:39], v200 offset:50176
	ds_read_b128 v[40:43], v200 offset:51200
	ds_read_b128 v[44:47], v200 offset:52224
	ds_read_b128 v[48:51], v200 offset:53248
	ds_read_b128 v[52:55], v200 offset:54272
	ds_read_b128 v[56:59], v200 offset:55296
	ds_read_b128 v[60:63], v200 offset:56320
	buffer_load_dwordx4 v194, s[60:63], s38 offen lds
	s_add_i32 s38, s42, s38
	s_mov_b32 m0, s84
	s_nop 0
	buffer_load_dwordx4 v194, s[60:63], s38 offen lds
	s_add_i32 s38, s38, s42
	s_mov_b32 m0, s87
	s_nop 0
	buffer_load_dwordx4 v194, s[60:63], s38 offen lds
	s_add_i32 s38, s38, s42
	s_mov_b32 m0, s90
	s_add_i32 s42, s42, s39
	buffer_load_dwordx4 v194, s[60:63], s38 offen lds
	s_mov_b32 m0, s85
	s_nop 0
	buffer_load_dwordx4 v192, s[60:63], s39 offen lds
	s_mov_b32 m0, s86
	s_nop 0
	buffer_load_dwordx4 v192, s[60:63], s42 offen lds
	s_waitcnt vmcnt(8)
	s_waitcnt lgkmcnt(0)
	s_barrier
	s_setprio 1
	s_waitcnt lgkmcnt(6)
	v_mfma_scale_f32_16x16x128_f8f6f4 v[124:127], v[0:7], v[32:39], v[124:127], v238, v238 op_sel_hi:[0,0,0]
	v_mfma_scale_f32_16x16x128_f8f6f4 v[120:123], v[8:15], v[32:39], v[120:123], v238, v238 op_sel_hi:[0,0,0]
	s_waitcnt lgkmcnt(4)
	v_mfma_scale_f32_16x16x128_f8f6f4 v[116:119], v[0:7], v[40:47], v[116:119], v238, v238 op_sel_hi:[0,0,0]
	v_mfma_scale_f32_16x16x128_f8f6f4 v[112:115], v[8:15], v[40:47], v[112:115], v238, v238 op_sel_hi:[0,0,0]
	s_waitcnt lgkmcnt(2)
	v_mfma_scale_f32_16x16x128_f8f6f4 v[108:111], v[0:7], v[48:55], v[108:111], v238, v238 op_sel_hi:[0,0,0]
	v_mfma_scale_f32_16x16x128_f8f6f4 v[104:107], v[8:15], v[48:55], v[104:107], v238, v238 op_sel_hi:[0,0,0]
	s_waitcnt lgkmcnt(0)
	v_mfma_scale_f32_16x16x128_f8f6f4 v[100:103], v[0:7], v[56:63], v[100:103], v238, v238 op_sel_hi:[0,0,0]
	v_mfma_scale_f32_16x16x128_f8f6f4 v[96:99], v[8:15], v[56:63], v[96:99], v238, v238 op_sel_hi:[0,0,0]
	s_setprio 0
	s_setprio 1
	v_mfma_scale_f32_16x16x128_f8f6f4 v[92:95], v[16:23], v[32:39], v[92:95], v238, v238 op_sel_hi:[0,0,0]
	v_mfma_scale_f32_16x16x128_f8f6f4 v[88:91], v[24:31], v[32:39], v[88:91], v238, v238 op_sel_hi:[0,0,0]
	v_mfma_scale_f32_16x16x128_f8f6f4 v[84:87], v[16:23], v[40:47], v[84:87], v238, v238 op_sel_hi:[0,0,0]
	v_mfma_scale_f32_16x16x128_f8f6f4 v[80:83], v[24:31], v[40:47], v[80:83], v238, v238 op_sel_hi:[0,0,0]
	v_mfma_scale_f32_16x16x128_f8f6f4 v[76:79], v[16:23], v[48:55], v[76:79], v238, v238 op_sel_hi:[0,0,0]
	v_mfma_scale_f32_16x16x128_f8f6f4 v[72:75], v[24:31], v[48:55], v[72:75], v238, v238 op_sel_hi:[0,0,0]
	v_mfma_scale_f32_16x16x128_f8f6f4 v[68:71], v[16:23], v[56:63], v[68:71], v238, v238 op_sel_hi:[0,0,0]
	v_mfma_scale_f32_16x16x128_f8f6f4 v[64:67], v[24:31], v[56:63], v[64:67], v238, v238 op_sel_hi:[0,0,0]
	s_add_i32 s82, s82, 2
	s_cmp_ge_u32 s82, s96
	s_setprio 0
	s_barrier
	s_cbranch_scc1 .LBB0_1464

.LBB0_1570:
	ds_read_b128 v[134:137], v132
	ds_read_b128 v[138:141], v132 offset:1024
	ds_read_b128 v[142:145], v132 offset:2048
	ds_read_b128 v[146:149], v132 offset:3072
	ds_read_b128 v[150:153], v132 offset:16384
	ds_read_b128 v[154:157], v132 offset:17408
	ds_read_b128 v[158:161], v132 offset:18432
	ds_read_b128 v[162:165], v132 offset:19456
	s_add_i32 s6, s42, 0xfffa0080
	s_cmp_eq_u32 s44, 12
	s_cselect_b32 s46, s40, s43
	s_cselect_b32 s45, s41, s6
	s_or_b32 s47, s46, 0x80
	s_add_i32 s6, s42, 0xfffe0000
	s_mov_b32 m0, s30
	ds_read_b128 v[166:169], v133
	ds_read_b128 v[170:173], v133 offset:1024
	ds_read_b128 v[174:177], v133 offset:2048
	ds_read_b128 v[178:181], v133 offset:3072
	ds_read_b128 v[182:185], v133 offset:4096
	ds_read_b128 v[186:189], v133 offset:5120
	ds_read_b128 v[190:193], v133 offset:6144
	ds_read_b128 v[194:197], v133 offset:7168
	buffer_load_dwordx4 v129, s[60:63], s6 offen lds
	s_mov_b32 m0, s31
	s_nop 0
	buffer_load_dwordx4 v129, s[60:63], s42 offen lds
	s_waitcnt vmcnt(8)
	s_waitcnt lgkmcnt(0)
	s_barrier
	s_setprio 1
	s_waitcnt lgkmcnt(7)
	v_mfma_f32_16x16x32_bf16 v[124:127], v[134:137], v[166:169], v[124:127]
	v_mfma_f32_16x16x32_bf16 v[116:119], v[142:145], v[166:169], v[116:119]
	s_waitcnt lgkmcnt(5)
	v_mfma_f32_16x16x32_bf16 v[108:111], v[134:137], v[174:177], v[108:111]
	v_mfma_f32_16x16x32_bf16 v[100:103], v[142:145], v[174:177], v[100:103]
	s_waitcnt lgkmcnt(3)
	v_mfma_f32_16x16x32_bf16 v[96:99], v[134:137], v[182:185], v[96:99]
	v_mfma_f32_16x16x32_bf16 v[84:87], v[142:145], v[182:185], v[84:87]
	s_waitcnt lgkmcnt(1)
	v_mfma_f32_16x16x32_bf16 v[80:83], v[134:137], v[190:193], v[80:83]
	v_mfma_f32_16x16x32_bf16 v[68:71], v[142:145], v[190:193], v[68:71]
	v_mfma_f32_16x16x32_bf16 v[124:127], v[138:141], v[170:173], v[124:127]
	v_mfma_f32_16x16x32_bf16 v[116:119], v[146:149], v[170:173], v[116:119]
	v_mfma_f32_16x16x32_bf16 v[108:111], v[138:141], v[178:181], v[108:111]
	v_mfma_f32_16x16x32_bf16 v[100:103], v[146:149], v[178:181], v[100:103]
	v_mfma_f32_16x16x32_bf16 v[96:99], v[138:141], v[186:189], v[96:99]
	v_mfma_f32_16x16x32_bf16 v[84:87], v[146:149], v[186:189], v[84:87]
	s_waitcnt lgkmcnt(0)
	v_mfma_f32_16x16x32_bf16 v[80:83], v[138:141], v[194:197], v[80:83]
	v_mfma_f32_16x16x32_bf16 v[68:71], v[146:149], v[194:197], v[68:71]
	s_setprio 0
	s_setprio 1
	v_mfma_f32_16x16x32_bf16 v[120:123], v[150:153], v[166:169], v[120:123]
	v_mfma_f32_16x16x32_bf16 v[112:115], v[158:161], v[166:169], v[112:115]
	v_mfma_f32_16x16x32_bf16 v[104:107], v[150:153], v[174:177], v[104:107]
	v_mfma_f32_16x16x32_bf16 v[92:95], v[158:161], v[174:177], v[92:95]
	v_mfma_f32_16x16x32_bf16 v[88:91], v[150:153], v[182:185], v[88:91]
	v_mfma_f32_16x16x32_bf16 v[76:79], v[158:161], v[182:185], v[76:79]
	v_mfma_f32_16x16x32_bf16 v[72:75], v[150:153], v[190:193], v[72:75]
	v_mfma_f32_16x16x32_bf16 v[64:67], v[158:161], v[190:193], v[64:67]
	v_mfma_f32_16x16x32_bf16 v[120:123], v[154:157], v[170:173], v[120:123]
	v_mfma_f32_16x16x32_bf16 v[112:115], v[162:165], v[170:173], v[112:115]
	v_mfma_f32_16x16x32_bf16 v[104:107], v[154:157], v[178:181], v[104:107]
	v_mfma_f32_16x16x32_bf16 v[92:95], v[162:165], v[178:181], v[92:95]
	v_mfma_f32_16x16x32_bf16 v[88:91], v[154:157], v[186:189], v[88:91]
	v_mfma_f32_16x16x32_bf16 v[76:79], v[162:165], v[186:189], v[76:79]
	v_mfma_f32_16x16x32_bf16 v[72:75], v[154:157], v[194:197], v[72:75]
	v_mfma_f32_16x16x32_bf16 v[64:67], v[162:165], v[194:197], v[64:67]
	s_setprio 0
	s_barrier
	s_mov_b32 m0, s15
	s_mov_b32 s6, s62
	s_mov_b32 s7, s63
	ds_read_b128 v[166:169], v133 offset:16384
	ds_read_b128 v[170:173], v133 offset:17408
	ds_read_b128 v[174:177], v133 offset:18432
	ds_read_b128 v[178:181], v133 offset:19456
	ds_read_b128 v[182:185], v133 offset:20480
	ds_read_b128 v[186:189], v133 offset:21504
	ds_read_b128 v[190:193], v133 offset:22528
	ds_read_b128 v[194:197], v133 offset:23552
	buffer_load_dwordx4 v130, s[4:7], s46 offen lds
	s_add_i32 s48, s46, 0x20000
	s_mov_b32 m0, s16
	s_nop 0
	buffer_load_dwordx4 v130, s[4:7], s48 offen lds
	s_add_i32 s48, s46, 0x40000
	s_mov_b32 m0, s17
	s_nop 0
	buffer_load_dwordx4 v130, s[4:7], s48 offen lds
	s_add_i32 s48, s46, 0x60000
	s_mov_b32 m0, s18
	s_nop 0
	buffer_load_dwordx4 v130, s[4:7], s48 offen lds
	s_mov_b32 m0, s14
	s_add_i32 s48, s45, 0x20000
	buffer_load_dwordx4 v129, s[60:63], s45 offen lds
	s_mov_b32 m0, s19
	s_nop 0
	buffer_load_dwordx4 v129, s[60:63], s48 offen lds
	s_waitcnt vmcnt(8)
	s_waitcnt lgkmcnt(0)
	s_barrier
	s_setprio 1
	s_waitcnt lgkmcnt(7)
	v_mfma_f32_16x16x32_bf16 v[60:63], v[134:137], v[166:169], v[60:63]
	v_mfma_f32_16x16x32_bf16 v[52:55], v[142:145], v[166:169], v[52:55]
	s_waitcnt lgkmcnt(5)
	v_mfma_f32_16x16x32_bf16 v[48:51], v[134:137], v[174:177], v[48:51]
	v_mfma_f32_16x16x32_bf16 v[36:39], v[142:145], v[174:177], v[36:39]
	s_waitcnt lgkmcnt(3)
	v_mfma_f32_16x16x32_bf16 v[32:35], v[134:137], v[182:185], v[32:35]
	v_mfma_f32_16x16x32_bf16 v[20:23], v[142:145], v[182:185], v[20:23]
	s_waitcnt lgkmcnt(1)
	v_mfma_f32_16x16x32_bf16 v[16:19], v[134:137], v[190:193], v[16:19]
	v_mfma_f32_16x16x32_bf16 v[4:7], v[142:145], v[190:193], v[4:7]
	v_mfma_f32_16x16x32_bf16 v[60:63], v[138:141], v[170:173], v[60:63]
	v_mfma_f32_16x16x32_bf16 v[52:55], v[146:149], v[170:173], v[52:55]
	v_mfma_f32_16x16x32_bf16 v[48:51], v[138:141], v[178:181], v[48:51]
	v_mfma_f32_16x16x32_bf16 v[36:39], v[146:149], v[178:181], v[36:39]
	v_mfma_f32_16x16x32_bf16 v[32:35], v[138:141], v[186:189], v[32:35]
	v_mfma_f32_16x16x32_bf16 v[20:23], v[146:149], v[186:189], v[20:23]
	s_waitcnt lgkmcnt(0)
	v_mfma_f32_16x16x32_bf16 v[16:19], v[138:141], v[194:197], v[16:19]
	v_mfma_f32_16x16x32_bf16 v[4:7], v[146:149], v[194:197], v[4:7]
	s_setprio 0
	s_setprio 1
	v_mfma_f32_16x16x32_bf16 v[56:59], v[150:153], v[166:169], v[56:59]
	v_mfma_f32_16x16x32_bf16 v[44:47], v[158:161], v[166:169], v[44:47]
	v_mfma_f32_16x16x32_bf16 v[40:43], v[150:153], v[174:177], v[40:43]
	v_mfma_f32_16x16x32_bf16 v[28:31], v[158:161], v[174:177], v[28:31]
	v_mfma_f32_16x16x32_bf16 v[24:27], v[150:153], v[182:185], v[24:27]
	v_mfma_f32_16x16x32_bf16 v[12:15], v[158:161], v[182:185], v[12:15]
	v_mfma_f32_16x16x32_bf16 v[8:11], v[150:153], v[190:193], v[8:11]
	v_mfma_f32_16x16x32_bf16 v[0:3], v[158:161], v[190:193], v[0:3]
	v_mfma_f32_16x16x32_bf16 v[56:59], v[154:157], v[170:173], v[56:59]
	v_mfma_f32_16x16x32_bf16 v[44:47], v[162:165], v[170:173], v[44:47]
	v_mfma_f32_16x16x32_bf16 v[40:43], v[154:157], v[178:181], v[40:43]
	v_mfma_f32_16x16x32_bf16 v[28:31], v[162:165], v[178:181], v[28:31]
	v_mfma_f32_16x16x32_bf16 v[24:27], v[154:157], v[186:189], v[24:27]
	v_mfma_f32_16x16x32_bf16 v[12:15], v[162:165], v[186:189], v[12:15]
	v_mfma_f32_16x16x32_bf16 v[8:11], v[154:157], v[194:197], v[8:11]
	v_mfma_f32_16x16x32_bf16 v[0:3], v[162:165], v[194:197], v[0:3]
	s_setprio 0
	s_barrier
	ds_read_b128 v[134:137], v132 offset:32768
	ds_read_b128 v[138:141], v132 offset:33792
	ds_read_b128 v[142:145], v132 offset:34816
	ds_read_b128 v[146:149], v132 offset:35840
	ds_read_b128 v[150:153], v132 offset:49152
	ds_read_b128 v[154:157], v132 offset:50176
	ds_read_b128 v[158:161], v132 offset:51200
	ds_read_b128 v[162:165], v132 offset:52224
	s_mov_b32 m0, s20
	s_add_i32 s48, s45, 0x40000
	ds_read_b128 v[166:169], v133 offset:32768
	ds_read_b128 v[170:173], v133 offset:33792
	ds_read_b128 v[174:177], v133 offset:34816
	ds_read_b128 v[178:181], v133 offset:35840
	ds_read_b128 v[182:185], v133 offset:36864
	ds_read_b128 v[186:189], v133 offset:37888
	ds_read_b128 v[190:193], v133 offset:38912
	ds_read_b128 v[194:197], v133 offset:39936
	buffer_load_dwordx4 v129, s[60:63], s48 offen lds
	s_add_i32 s48, s45, 0x60000
	s_mov_b32 m0, s21
	s_nop 0
	buffer_load_dwordx4 v129, s[60:63], s48 offen lds
	s_waitcnt vmcnt(8)
	s_waitcnt lgkmcnt(0)
	s_barrier
	s_setprio 1
	s_waitcnt lgkmcnt(7)
	v_mfma_f32_16x16x32_bf16 v[124:127], v[134:137], v[166:169], v[124:127]
	v_mfma_f32_16x16x32_bf16 v[116:119], v[142:145], v[166:169], v[116:119]
	s_waitcnt lgkmcnt(5)
	v_mfma_f32_16x16x32_bf16 v[108:111], v[134:137], v[174:177], v[108:111]
	v_mfma_f32_16x16x32_bf16 v[100:103], v[142:145], v[174:177], v[100:103]
	s_waitcnt lgkmcnt(3)
	v_mfma_f32_16x16x32_bf16 v[96:99], v[134:137], v[182:185], v[96:99]
	v_mfma_f32_16x16x32_bf16 v[84:87], v[142:145], v[182:185], v[84:87]
	s_waitcnt lgkmcnt(1)
	v_mfma_f32_16x16x32_bf16 v[80:83], v[134:137], v[190:193], v[80:83]
	v_mfma_f32_16x16x32_bf16 v[68:71], v[142:145], v[190:193], v[68:71]
	v_mfma_f32_16x16x32_bf16 v[124:127], v[138:141], v[170:173], v[124:127]
	v_mfma_f32_16x16x32_bf16 v[116:119], v[146:149], v[170:173], v[116:119]
	v_mfma_f32_16x16x32_bf16 v[108:111], v[138:141], v[178:181], v[108:111]
	v_mfma_f32_16x16x32_bf16 v[100:103], v[146:149], v[178:181], v[100:103]
	v_mfma_f32_16x16x32_bf16 v[96:99], v[138:141], v[186:189], v[96:99]
	v_mfma_f32_16x16x32_bf16 v[84:87], v[146:149], v[186:189], v[84:87]
	s_waitcnt lgkmcnt(0)
	v_mfma_f32_16x16x32_bf16 v[80:83], v[138:141], v[194:197], v[80:83]
	v_mfma_f32_16x16x32_bf16 v[68:71], v[146:149], v[194:197], v[68:71]
	s_setprio 0
	s_setprio 1
	v_mfma_f32_16x16x32_bf16 v[120:123], v[150:153], v[166:169], v[120:123]
	v_mfma_f32_16x16x32_bf16 v[112:115], v[158:161], v[166:169], v[112:115]
	v_mfma_f32_16x16x32_bf16 v[104:107], v[150:153], v[174:177], v[104:107]
	v_mfma_f32_16x16x32_bf16 v[92:95], v[158:161], v[174:177], v[92:95]
	v_mfma_f32_16x16x32_bf16 v[88:91], v[150:153], v[182:185], v[88:91]
	v_mfma_f32_16x16x32_bf16 v[76:79], v[158:161], v[182:185], v[76:79]
	v_mfma_f32_16x16x32_bf16 v[72:75], v[150:153], v[190:193], v[72:75]
	v_mfma_f32_16x16x32_bf16 v[64:67], v[158:161], v[190:193], v[64:67]
	v_mfma_f32_16x16x32_bf16 v[120:123], v[154:157], v[170:173], v[120:123]
	v_mfma_f32_16x16x32_bf16 v[112:115], v[162:165], v[170:173], v[112:115]
	v_mfma_f32_16x16x32_bf16 v[104:107], v[154:157], v[178:181], v[104:107]
	v_mfma_f32_16x16x32_bf16 v[92:95], v[162:165], v[178:181], v[92:95]
	v_mfma_f32_16x16x32_bf16 v[88:91], v[154:157], v[186:189], v[88:91]
	v_mfma_f32_16x16x32_bf16 v[76:79], v[162:165], v[186:189], v[76:79]
	v_mfma_f32_16x16x32_bf16 v[72:75], v[154:157], v[194:197], v[72:75]
	v_mfma_f32_16x16x32_bf16 v[64:67], v[162:165], v[194:197], v[64:67]
	s_setprio 0
	s_barrier
	s_mov_b32 m0, s22
	ds_read_b128 v[166:169], v133 offset:49152
	ds_read_b128 v[170:173], v133 offset:50176
	ds_read_b128 v[174:177], v133 offset:51200
	ds_read_b128 v[178:181], v133 offset:52224
	ds_read_b128 v[182:185], v133 offset:53248
	ds_read_b128 v[186:189], v133 offset:54272
	ds_read_b128 v[190:193], v133 offset:55296
	ds_read_b128 v[194:197], v133 offset:56320
	buffer_load_dwordx4 v130, s[4:7], s47 offen lds
	s_add_i32 s47, s46, 0x20080
	s_mov_b32 m0, s23
	s_or_b32 s48, s45, 0x80
	buffer_load_dwordx4 v130, s[4:7], s47 offen lds
	s_add_i32 s47, s46, 0x40080
	s_mov_b32 m0, s26
	s_add_i32 s46, s46, 0x60080
	buffer_load_dwordx4 v130, s[4:7], s47 offen lds
	s_mov_b32 m0, s27
	s_add_i32 s45, s45, 0x20080
	buffer_load_dwordx4 v130, s[4:7], s46 offen lds
	s_mov_b32 m0, s24
	s_nop 0
	buffer_load_dwordx4 v129, s[60:63], s48 offen lds
	s_mov_b32 m0, s25
	s_nop 0
	buffer_load_dwordx4 v129, s[60:63], s45 offen lds
	s_waitcnt vmcnt(8)
	s_waitcnt lgkmcnt(0)
	s_barrier
	s_setprio 1
	s_waitcnt lgkmcnt(7)
	v_mfma_f32_16x16x32_bf16 v[60:63], v[134:137], v[166:169], v[60:63]
	v_mfma_f32_16x16x32_bf16 v[52:55], v[142:145], v[166:169], v[52:55]
	s_waitcnt lgkmcnt(5)
	v_mfma_f32_16x16x32_bf16 v[48:51], v[134:137], v[174:177], v[48:51]
	v_mfma_f32_16x16x32_bf16 v[36:39], v[142:145], v[174:177], v[36:39]
	s_waitcnt lgkmcnt(3)
	v_mfma_f32_16x16x32_bf16 v[32:35], v[134:137], v[182:185], v[32:35]
	v_mfma_f32_16x16x32_bf16 v[20:23], v[142:145], v[182:185], v[20:23]
	s_waitcnt lgkmcnt(1)
	v_mfma_f32_16x16x32_bf16 v[16:19], v[134:137], v[190:193], v[16:19]
	v_mfma_f32_16x16x32_bf16 v[4:7], v[142:145], v[190:193], v[4:7]
	v_mfma_f32_16x16x32_bf16 v[60:63], v[138:141], v[170:173], v[60:63]
	v_mfma_f32_16x16x32_bf16 v[52:55], v[146:149], v[170:173], v[52:55]
	v_mfma_f32_16x16x32_bf16 v[48:51], v[138:141], v[178:181], v[48:51]
	v_mfma_f32_16x16x32_bf16 v[36:39], v[146:149], v[178:181], v[36:39]
	v_mfma_f32_16x16x32_bf16 v[32:35], v[138:141], v[186:189], v[32:35]
	v_mfma_f32_16x16x32_bf16 v[20:23], v[146:149], v[186:189], v[20:23]
	s_waitcnt lgkmcnt(0)
	v_mfma_f32_16x16x32_bf16 v[16:19], v[138:141], v[194:197], v[16:19]
	v_mfma_f32_16x16x32_bf16 v[4:7], v[146:149], v[194:197], v[4:7]
	s_setprio 0
	s_setprio 1
	v_mfma_f32_16x16x32_bf16 v[56:59], v[150:153], v[166:169], v[56:59]
	v_mfma_f32_16x16x32_bf16 v[44:47], v[158:161], v[166:169], v[44:47]
	v_mfma_f32_16x16x32_bf16 v[40:43], v[150:153], v[174:177], v[40:43]
	v_mfma_f32_16x16x32_bf16 v[28:31], v[158:161], v[174:177], v[28:31]
	v_mfma_f32_16x16x32_bf16 v[24:27], v[150:153], v[182:185], v[24:27]
	v_mfma_f32_16x16x32_bf16 v[12:15], v[158:161], v[182:185], v[12:15]
	v_mfma_f32_16x16x32_bf16 v[8:11], v[150:153], v[190:193], v[8:11]
	v_mfma_f32_16x16x32_bf16 v[0:3], v[158:161], v[190:193], v[0:3]
	v_mfma_f32_16x16x32_bf16 v[56:59], v[154:157], v[170:173], v[56:59]
	v_mfma_f32_16x16x32_bf16 v[44:47], v[162:165], v[170:173], v[44:47]
	v_mfma_f32_16x16x32_bf16 v[40:43], v[154:157], v[178:181], v[40:43]
	v_mfma_f32_16x16x32_bf16 v[28:31], v[162:165], v[178:181], v[28:31]
	v_mfma_f32_16x16x32_bf16 v[24:27], v[154:157], v[186:189], v[24:27]
	v_mfma_f32_16x16x32_bf16 v[12:15], v[162:165], v[186:189], v[12:15]
	v_mfma_f32_16x16x32_bf16 v[8:11], v[154:157], v[194:197], v[8:11]
	v_mfma_f32_16x16x32_bf16 v[0:3], v[162:165], v[194:197], v[0:3]
	s_add_i32 s44, s44, 2
	s_addk_i32 s42, 0x100
	s_addk_i32 s43, 0x100
	s_cmp_gt_u32 s44, 13
	s_setprio 0
	s_barrier
	s_cbranch_scc0 .LBB0_1570
	s_and_b64 vcc, exec, s[12:13]
	s_cbranch_vccz .LBB0_1573
	s_barrier

.LBB0_1646:
	ds_read_b128 v[128:131], v245
	ds_read_b128 v[132:135], v245 offset:1024
	ds_read_b128 v[136:139], v245 offset:2048
	ds_read_b128 v[140:143], v245 offset:3072
	ds_read_b128 v[144:147], v245 offset:16384
	ds_read_b128 v[148:151], v245 offset:17408
	ds_read_b128 v[152:155], v245 offset:18432
	ds_read_b128 v[156:159], v245 offset:19456
	s_add_i32 s10, s12, 0xfff7c080
	s_cmp_eq_u32 s14, 18
	s_cselect_b32 s36, s2, s13
	s_cselect_b32 s15, s3, s10
	s_or_b32 s37, s36, 0x80
	s_add_i32 s10, s12, 0xfffd4000
	s_mov_b32 m0, s59
	ds_read_b128 v[160:163], v246
	ds_read_b128 v[164:167], v246 offset:1024
	ds_read_b128 v[168:171], v246 offset:2048
	ds_read_b128 v[172:175], v246 offset:3072
	ds_read_b128 v[176:179], v246 offset:4096
	ds_read_b128 v[180:183], v246 offset:5120
	ds_read_b128 v[184:187], v246 offset:6144
	ds_read_b128 v[188:191], v246 offset:7168
	buffer_load_dwordx4 v243, s[4:7], s10 offen lds
	s_mov_b32 m0, s66
	s_nop 0
	buffer_load_dwordx4 v243, s[4:7], s12 offen lds
	s_waitcnt vmcnt(8)
	s_waitcnt lgkmcnt(0)
	s_barrier
	s_setprio 1
	s_waitcnt lgkmcnt(0)
	v_mfma_scale_f32_16x16x128_f8f6f4 v[56:59], v[128:135], v[168:175], v[56:59], v238, v238 op_sel_hi:[0,0,0]
	v_mfma_scale_f32_16x16x128_f8f6f4 v[64:67], v[136:143], v[168:175], v[64:67], v238, v238 op_sel_hi:[0,0,0]
	v_mfma_scale_f32_16x16x128_f8f6f4 v[192:195], v[128:135], v[160:167], v[28:31], v238, v238 op_sel_hi:[0,0,0]
	v_mfma_scale_f32_16x16x128_f8f6f4 v[196:199], v[136:143], v[160:167], v[32:35], v238, v238 op_sel_hi:[0,0,0]
	s_waitcnt lgkmcnt(2)
	v_mfma_scale_f32_16x16x128_f8f6f4 v[200:203], v[128:135], v[176:183], v[88:91], v238, v238 op_sel_hi:[0,0,0]
	v_mfma_scale_f32_16x16x128_f8f6f4 v[204:207], v[136:143], v[176:183], v[92:95], v238, v238 op_sel_hi:[0,0,0]
	s_waitcnt lgkmcnt(0)
	v_mfma_scale_f32_16x16x128_f8f6f4 v[212:215], v[128:135], v[184:191], v[116:119], v238, v238 op_sel_hi:[0,0,0]
	v_mfma_scale_f32_16x16x128_f8f6f4 v[216:219], v[136:143], v[184:191], v[120:123], v238, v238 op_sel_hi:[0,0,0]
	s_setprio 0
	s_setprio 1
	v_mfma_scale_f32_16x16x128_f8f6f4 v[40:43], v[144:151], v[160:167], v[40:43], v238, v238 op_sel_hi:[0,0,0]
	v_mfma_scale_f32_16x16x128_f8f6f4 v[48:51], v[152:159], v[160:167], v[48:51], v238, v238 op_sel_hi:[0,0,0]
	v_mfma_scale_f32_16x16x128_f8f6f4 v[72:75], v[144:151], v[168:175], v[72:75], v238, v238 op_sel_hi:[0,0,0]
	v_mfma_scale_f32_16x16x128_f8f6f4 v[100:103], v[144:151], v[176:183], v[100:103], v238, v238 op_sel_hi:[0,0,0]
	v_mfma_scale_f32_16x16x128_f8f6f4 v[124:127], v[144:151], v[184:191], v[124:127], v238, v238 op_sel_hi:[0,0,0]
	v_mfma_scale_f32_16x16x128_f8f6f4 v[160:163], v[152:159], v[168:175], v[80:83], v238, v238 op_sel_hi:[0,0,0]
	v_mfma_scale_f32_16x16x128_f8f6f4 v[164:167], v[152:159], v[176:183], v[108:111], v238, v238 op_sel_hi:[0,0,0]
	v_mfma_scale_f32_16x16x128_f8f6f4 v[168:171], v[152:159], v[184:191], v[112:115], v238, v238 op_sel_hi:[0,0,0]
	s_setprio 0
	s_barrier
	s_mov_b32 m0, s43
	s_mov_b32 s10, s6
	s_mov_b32 s11, s7
	ds_read_b128 v[28:31], v246 offset:16384
	ds_read_b128 v[32:35], v246 offset:17408
	ds_read_b128 v[88:91], v246 offset:18432
	ds_read_b128 v[92:95], v246 offset:19456
	ds_read_b128 v[108:111], v246 offset:20480
	ds_read_b128 v[112:115], v246 offset:21504
	ds_read_b128 v[116:119], v246 offset:22528
	ds_read_b128 v[120:123], v246 offset:23552
	buffer_load_dwordx4 v243, s[8:11], s36 offen lds
	s_add_i32 s38, s36, 0x2c000
	s_mov_b32 m0, s44
	s_nop 0
	buffer_load_dwordx4 v243, s[8:11], s38 offen lds
	s_add_i32 s38, s36, 0x58000
	s_mov_b32 m0, s45
	s_nop 0
	buffer_load_dwordx4 v243, s[8:11], s38 offen lds
	s_add_i32 s38, s36, 0x84000
	s_mov_b32 m0, s47
	s_nop 0
	buffer_load_dwordx4 v243, s[8:11], s38 offen lds
	s_mov_b32 m0, s42
	s_add_i32 s38, s15, 0x2c000
	buffer_load_dwordx4 v243, s[4:7], s15 offen lds
	s_mov_b32 m0, s48
	s_nop 0
	buffer_load_dwordx4 v243, s[4:7], s38 offen lds
	s_waitcnt vmcnt(8)
	s_waitcnt lgkmcnt(0)
	s_barrier
	s_setprio 1
	s_waitcnt lgkmcnt(0)
	v_mfma_scale_f32_16x16x128_f8f6f4 v[96:99], v[136:143], v[28:35], v[96:99], v238, v238 op_sel_hi:[0,0,0]
	s_waitcnt lgkmcnt(4)
	v_mfma_scale_f32_16x16x128_f8f6f4 v[68:71], v[128:135], v[88:95], v[68:71], v238, v238 op_sel_hi:[0,0,0]
	v_mfma_scale_f32_16x16x128_f8f6f4 v[60:63], v[136:143], v[88:95], v[60:63], v238, v238 op_sel_hi:[0,0,0]
	s_waitcnt lgkmcnt(2)
	v_mfma_scale_f32_16x16x128_f8f6f4 v[36:39], v[128:135], v[108:115], v[36:39], v238, v238 op_sel_hi:[0,0,0]
	v_mfma_scale_f32_16x16x128_f8f6f4 v[24:27], v[136:143], v[108:115], v[24:27], v238, v238 op_sel_hi:[0,0,0]
	v_mfma_scale_f32_16x16x128_f8f6f4 v[176:179], v[128:135], v[28:35], v[104:107], v238, v238 op_sel_hi:[0,0,0]
	s_waitcnt lgkmcnt(0)
	v_mfma_scale_f32_16x16x128_f8f6f4 v[180:183], v[128:135], v[116:123], v[12:15], v238, v238 op_sel_hi:[0,0,0]
	v_mfma_scale_f32_16x16x128_f8f6f4 v[184:187], v[136:143], v[116:123], v[8:11], v238, v238 op_sel_hi:[0,0,0]
	s_setprio 0
	s_setprio 1
	v_mfma_scale_f32_16x16x128_f8f6f4 v[84:87], v[144:151], v[28:35], v[84:87], v238, v238 op_sel_hi:[0,0,0]
	v_mfma_scale_f32_16x16x128_f8f6f4 v[52:55], v[144:151], v[88:95], v[52:55], v238, v238 op_sel_hi:[0,0,0]
	v_mfma_scale_f32_16x16x128_f8f6f4 v[44:47], v[152:159], v[88:95], v[44:47], v238, v238 op_sel_hi:[0,0,0]
	v_mfma_scale_f32_16x16x128_f8f6f4 v[188:191], v[152:159], v[28:35], v[76:79], v238, v238 op_sel_hi:[0,0,0]
	v_mfma_scale_f32_16x16x128_f8f6f4 v[220:223], v[144:151], v[108:115], v[20:23], v238, v238 op_sel_hi:[0,0,0]
	v_mfma_scale_f32_16x16x128_f8f6f4 v[224:227], v[152:159], v[108:115], v[16:19], v238, v238 op_sel_hi:[0,0,0]
	v_mfma_scale_f32_16x16x128_f8f6f4 v[228:231], v[144:151], v[116:123], v[4:7], v238, v238 op_sel_hi:[0,0,0]
	v_mfma_scale_f32_16x16x128_f8f6f4 v[232:235], v[152:159], v[116:123], v[0:3], v238, v238 op_sel_hi:[0,0,0]
	s_setprio 0
	s_barrier
	s_nop 4
	ds_read_b128 v[0:3], v245 offset:32768
	ds_read_b128 v[4:7], v245 offset:33792
	ds_read_b128 v[16:19], v245 offset:34816
	ds_read_b128 v[20:23], v245 offset:35840
	ds_read_b128 v[128:131], v245 offset:49152
	ds_read_b128 v[132:135], v245 offset:50176
	ds_read_b128 v[136:139], v245 offset:51200
	ds_read_b128 v[140:143], v245 offset:52224
	s_mov_b32 m0, s49
	s_add_i32 s38, s15, 0x58000
	ds_read_b128 v[8:11], v246 offset:32768
	ds_read_b128 v[12:15], v246 offset:33792
	ds_read_b128 v[76:79], v246 offset:34816
	ds_read_b128 v[80:83], v246 offset:35840
	ds_read_b128 v[104:107], v246 offset:36864
	ds_read_b128 v[108:111], v246 offset:37888
	ds_read_b128 v[144:147], v246 offset:38912
	ds_read_b128 v[148:151], v246 offset:39936
	buffer_load_dwordx4 v243, s[4:7], s38 offen lds
	s_add_i32 s38, s15, 0x84000
	s_mov_b32 m0, s50
	s_nop 0
	buffer_load_dwordx4 v243, s[4:7], s38 offen lds
	s_waitcnt vmcnt(8)
	s_waitcnt lgkmcnt(0)
	s_barrier
	s_setprio 1
	s_waitcnt lgkmcnt(0)
	v_mfma_scale_f32_16x16x128_f8f6f4 v[28:31], v[0:7], v[8:15], v[192:195], v238, v238 op_sel_hi:[0,0,0]
	v_mfma_scale_f32_16x16x128_f8f6f4 v[32:35], v[16:23], v[8:15], v[196:199], v238, v238 op_sel_hi:[0,0,0]
	s_waitcnt lgkmcnt(4)
	v_mfma_scale_f32_16x16x128_f8f6f4 v[56:59], v[0:7], v[76:83], v[56:59], v238, v238 op_sel_hi:[0,0,0]
	v_mfma_scale_f32_16x16x128_f8f6f4 v[64:67], v[16:23], v[76:83], v[64:67], v238, v238 op_sel_hi:[0,0,0]
	s_waitcnt lgkmcnt(2)
	v_mfma_scale_f32_16x16x128_f8f6f4 v[88:91], v[0:7], v[104:111], v[200:203], v238, v238 op_sel_hi:[0,0,0]
	v_mfma_scale_f32_16x16x128_f8f6f4 v[92:95], v[16:23], v[104:111], v[204:207], v238, v238 op_sel_hi:[0,0,0]
	s_waitcnt lgkmcnt(0)
	v_mfma_scale_f32_16x16x128_f8f6f4 v[116:119], v[0:7], v[144:151], v[212:215], v238, v238 op_sel_hi:[0,0,0]
	v_mfma_scale_f32_16x16x128_f8f6f4 v[120:123], v[16:23], v[144:151], v[216:219], v238, v238 op_sel_hi:[0,0,0]
	s_setprio 0
	s_setprio 1
	v_mfma_scale_f32_16x16x128_f8f6f4 v[40:43], v[128:135], v[8:15], v[40:43], v238, v238 op_sel_hi:[0,0,0]
	v_mfma_scale_f32_16x16x128_f8f6f4 v[48:51], v[136:143], v[8:15], v[48:51], v238, v238 op_sel_hi:[0,0,0]
	v_mfma_scale_f32_16x16x128_f8f6f4 v[72:75], v[128:135], v[76:83], v[72:75], v238, v238 op_sel_hi:[0,0,0]
	v_mfma_scale_f32_16x16x128_f8f6f4 v[80:83], v[136:143], v[76:83], v[160:163], v238, v238 op_sel_hi:[0,0,0]
	v_mfma_scale_f32_16x16x128_f8f6f4 v[100:103], v[128:135], v[104:111], v[100:103], v238, v238 op_sel_hi:[0,0,0]
	v_mfma_scale_f32_16x16x128_f8f6f4 v[108:111], v[136:143], v[104:111], v[164:167], v238, v238 op_sel_hi:[0,0,0]
	v_mfma_scale_f32_16x16x128_f8f6f4 v[124:127], v[128:135], v[144:151], v[124:127], v238, v238 op_sel_hi:[0,0,0]
	v_mfma_scale_f32_16x16x128_f8f6f4 v[112:115], v[136:143], v[144:151], v[168:171], v238, v238 op_sel_hi:[0,0,0]
	s_setprio 0
	s_barrier
	s_mov_b32 m0, s51
	ds_read_b128 v[144:147], v246 offset:49152
	ds_read_b128 v[148:151], v246 offset:50176
	ds_read_b128 v[152:155], v246 offset:51200
	ds_read_b128 v[156:159], v246 offset:52224
	ds_read_b128 v[160:163], v246 offset:53248
	ds_read_b128 v[164:167], v246 offset:54272
	ds_read_b128 v[168:171], v246 offset:55296
	ds_read_b128 v[172:175], v246 offset:56320
	buffer_load_dwordx4 v243, s[8:11], s37 offen lds
	s_add_i32 s37, s36, 0x2c080
	s_mov_b32 m0, s52
	s_or_b32 s38, s15, 0x80
	buffer_load_dwordx4 v243, s[8:11], s37 offen lds
	s_add_i32 s37, s36, 0x58080
	s_mov_b32 m0, s55
	s_add_i32 s36, s36, 0x84080
	buffer_load_dwordx4 v243, s[8:11], s37 offen lds
	s_mov_b32 m0, s56
	s_add_i32 s15, s15, 0x2c080
	buffer_load_dwordx4 v243, s[8:11], s36 offen lds
	s_mov_b32 m0, s53
	s_nop 0
	buffer_load_dwordx4 v243, s[4:7], s38 offen lds
	s_mov_b32 m0, s54
	s_nop 0
	buffer_load_dwordx4 v243, s[4:7], s15 offen lds
	s_waitcnt vmcnt(8)
	s_waitcnt lgkmcnt(0)
	s_barrier
	s_setprio 1
	s_waitcnt lgkmcnt(0)
	v_mfma_scale_f32_16x16x128_f8f6f4 v[104:107], v[0:7], v[144:151], v[176:179], v238, v238 op_sel_hi:[0,0,0]
	v_mfma_scale_f32_16x16x128_f8f6f4 v[96:99], v[16:23], v[144:151], v[96:99], v238, v238 op_sel_hi:[0,0,0]
	s_waitcnt lgkmcnt(4)
	v_mfma_scale_f32_16x16x128_f8f6f4 v[68:71], v[0:7], v[152:159], v[68:71], v238, v238 op_sel_hi:[0,0,0]
	v_mfma_scale_f32_16x16x128_f8f6f4 v[60:63], v[16:23], v[152:159], v[60:63], v238, v238 op_sel_hi:[0,0,0]
	s_waitcnt lgkmcnt(2)
	v_mfma_scale_f32_16x16x128_f8f6f4 v[36:39], v[0:7], v[160:167], v[36:39], v238, v238 op_sel_hi:[0,0,0]
	v_mfma_scale_f32_16x16x128_f8f6f4 v[24:27], v[16:23], v[160:167], v[24:27], v238, v238 op_sel_hi:[0,0,0]
	s_waitcnt lgkmcnt(0)
	v_mfma_scale_f32_16x16x128_f8f6f4 v[12:15], v[0:7], v[168:175], v[180:183], v238, v238 op_sel_hi:[0,0,0]
	v_mfma_scale_f32_16x16x128_f8f6f4 v[8:11], v[16:23], v[168:175], v[184:187], v238, v238 op_sel_hi:[0,0,0]
	s_setprio 0
	s_setprio 1
	v_mfma_scale_f32_16x16x128_f8f6f4 v[84:87], v[128:135], v[144:151], v[84:87], v238, v238 op_sel_hi:[0,0,0]
	v_mfma_scale_f32_16x16x128_f8f6f4 v[76:79], v[136:143], v[144:151], v[188:191], v238, v238 op_sel_hi:[0,0,0]
	v_mfma_scale_f32_16x16x128_f8f6f4 v[52:55], v[128:135], v[152:159], v[52:55], v238, v238 op_sel_hi:[0,0,0]
	v_mfma_scale_f32_16x16x128_f8f6f4 v[44:47], v[136:143], v[152:159], v[44:47], v238, v238 op_sel_hi:[0,0,0]
	v_mfma_scale_f32_16x16x128_f8f6f4 v[20:23], v[128:135], v[160:167], v[220:223], v238, v238 op_sel_hi:[0,0,0]
	v_mfma_scale_f32_16x16x128_f8f6f4 v[16:19], v[136:143], v[160:167], v[224:227], v238, v238 op_sel_hi:[0,0,0]
	v_mfma_scale_f32_16x16x128_f8f6f4 v[4:7], v[128:135], v[168:175], v[228:231], v238, v238 op_sel_hi:[0,0,0]
	v_mfma_scale_f32_16x16x128_f8f6f4 v[0:3], v[136:143], v[168:175], v[232:235], v238, v238 op_sel_hi:[0,0,0]
	s_add_i32 s14, s14, 2
	s_addk_i32 s12, 0x100
	s_addk_i32 s13, 0x100
	s_cmp_gt_u32 s14, 19
	s_setprio 0
	s_barrier
	s_cbranch_scc0 .LBB0_1646
	s_and_b64 vcc, exec, s[22:23]
	s_cbranch_vccz .LBB0_1649
	s_barrier
